# speedup vs baseline: 1.0121x; 1.0052x over previous
_Z12k1_colsum_q8PKfPjPfS2_:
	s_load_dwordx8 s[4:11], s[0:1], 0x0
	v_and_b32_e32 v1, 63, v0
	v_lshrrev_b32_e32 v41, 6, v0
	s_and_b32 s12, s2, 7
	s_lshl_b32 s12, s12, 6
	s_lshr_b32 s13, s2, 3
	s_or_b32 s12, s12, s13
	s_lshl_b32 s12, s12, 3
	v_readfirstlane_b32 s14, v41
	s_add_u32 s12, s12, s14
	s_cmp_lt_u32 s12, 0x6a0
	s_cselect_b32 s29, 1, 0
	v_lshlrev_b32_e32 v34, 4, v1
	v_min_u32_e32 v35, 57, v1
	v_lshlrev_b32_e32 v35, 4, v35
	v_cmp_gt_u32_e64 s[18:19], 58, v1
	s_lshl_b32 s35, s14, 13
	s_add_u32 s36, s35, 0x1000
	v_add_u32_e32 v38, s35, v34
	v_lshrrev_b32_e32 v41, 5, v1
	v_mov_b32_e32 v42, 0xc35000
	v_mul_lo_u32 v39, v41, v42
	v_and_b32_e32 v42, 31, v1
	v_lshl_add_u32 v39, v42, 2, v39
	v_mov_b32_e32 v2, 0
	v_mov_b32_e32 v3, 0
	v_mov_b32_e32 v4, 0
	v_mov_b32_e32 v5, 0
	v_mov_b32_e32 v6, 0
	v_mov_b32_e32 v7, 0
	v_mov_b32_e32 v8, 0
	v_mov_b32_e32 v9, 0
	v_mov_b32_e32 v10, 0
	v_mov_b32_e32 v11, 0
	v_mov_b32_e32 v12, 0
	v_mov_b32_e32 v13, 0
	v_mov_b32_e32 v14, 0
	v_mov_b32_e32 v15, 0
	v_mov_b32_e32 v16, 0
	v_mov_b32_e32 v17, 0
	v_mov_b32_e32 v40, 0
	v_mov_b32_e32 v47, 0x42fe0000
	s_mov_b32 s32, 0x42fe0000
	s_mov_b32 s33, 0xc0c0400
	s_mov_b32 s34, 0x4000c0c
	s_mov_b32 s15, s12
	s_mul_i32 s37, s15, 0xfa0
	s_lshl_b32 s15, s15, 7
	s_waitcnt lgkmcnt(0)
	s_add_u32 s16, s4, s37
	s_addc_u32 s17, s5, 0
	s_add_u32 s40, s6, s15
	s_addc_u32 s41, s7, 0
	s_add_u32 s20, s40, 0
	s_addc_u32 s21, s41, 0
	s_add_u32 s22, s20, 0x186a000
	s_addc_u32 s23, s21, 0
	s_add_u32 s24, s22, 0x186a000
	s_addc_u32 s25, s23, 0
	s_add_u32 s26, s24, 0x186a000
	s_addc_u32 s27, s25, 0
	s_mov_b32 m0, s35
	s_nop 0
	global_load_lds_dwordx4 v34, s[16:17] nt
	global_load_lds_dwordx4 v34, s[16:17] offset:1024 nt
	global_load_lds_dwordx4 v34, s[16:17] offset:2048 nt
	global_load_lds_dwordx4 v35, s[16:17] offset:3072 nt
	s_add_u32 s16, s16, 0xfa0000
	s_addc_u32 s17, s17, 0
	s_waitcnt vmcnt(0)
	ds_read_b128 v[18:21], v38 offset:0
	ds_read_b128 v[22:25], v38 offset:1024
	ds_read_b128 v[26:29], v38 offset:2048
	ds_read_b128 v[30:33], v38 offset:3072
	s_waitcnt lgkmcnt(0)
	s_barrier
	s_mov_b32 m0, s35
	s_nop 0
	global_load_lds_dwordx4 v34, s[16:17] nt
	global_load_lds_dwordx4 v34, s[16:17] offset:1024 nt
	global_load_lds_dwordx4 v34, s[16:17] offset:2048 nt
	global_load_lds_dwordx4 v35, s[16:17] offset:3072 nt
	s_add_u32 s16, s16, 0xfa0000
	s_addc_u32 s17, s17, 0
	v_cndmask_b32_e64 v30, 0, v30, s[18:19]
	v_cndmask_b32_e64 v31, 0, v31, s[18:19]
	v_cndmask_b32_e64 v32, 0, v32, s[18:19]
	v_cndmask_b32_e64 v33, 0, v33, s[18:19]
	v_max3_f32 v41, |v18|, |v19|, |v20|
	v_max3_f32 v42, |v21|, |v22|, |v23|
	v_max3_f32 v43, |v24|, |v25|, |v26|
	v_max3_f32 v44, |v27|, |v28|, |v29|
	v_max3_f32 v48, |v30|, |v31|, |v32|
	v_max3_f32 v41, v41, v42, |v33|
	v_max3_f32 v43, v43, v44, v48
	v_max_f32_e32 v41, v41, v43
	v_pk_add_f32 v[2:3], v[2:3], v[18:19]
	v_pk_add_f32 v[4:5], v[4:5], v[20:21]
	v_max_f32_dpp v41, v41, v41 quad_perm:[1,0,3,2] row_mask:0xf bank_mask:0xf
	v_pk_add_f32 v[6:7], v[6:7], v[22:23]
	v_pk_add_f32 v[8:9], v[8:9], v[24:25]
	v_max_f32_dpp v41, v41, v41 quad_perm:[2,3,0,1] row_mask:0xf bank_mask:0xf
	v_pk_add_f32 v[10:11], v[10:11], v[26:27]
	v_pk_add_f32 v[12:13], v[12:13], v[28:29]
	v_max_f32_dpp v41, v41, v41 row_half_mirror row_mask:0xf bank_mask:0xf
	v_pk_add_f32 v[14:15], v[14:15], v[30:31]
	v_pk_add_f32 v[16:17], v[16:17], v[32:33]
	v_max_f32_dpp v41, v41, v41 row_mirror row_mask:0xf bank_mask:0xf
	s_nop 1
	v_max_f32_dpp v41, v41, v41 row_bcast:15 row_mask:0xa bank_mask:0xf
	s_nop 1
	v_max_f32_dpp v41, v41, v41 row_bcast:31 row_mask:0xc bank_mask:0xf
	s_nop 1
	v_readlane_b32 s28, v41, 63
	s_nop 1
	v_div_scale_f32 v48, s[30:31], s28, s28, v47
	v_rcp_f32_e32 v49, v48
	s_nop 0
	v_fma_f32 v50, -v48, v49, 1.0
	v_fmac_f32_e32 v49, v50, v49
	v_mov_b32_e32 v50, s28
	v_div_scale_f32 v50, vcc, s32, v50, s32
	v_mul_f32_e32 v51, v50, v49
	v_fma_f32 v52, -v48, v51, v50
	v_fmac_f32_e32 v51, v52, v49
	v_fma_f32 v48, -v48, v51, v50
	v_div_fmas_f32 v48, v48, v49, v51
	v_div_fixup_f32 v48, v48, s28, v47
	v_cmp_gt_f32_e64 vcc, s28, 0
	v_writelane_b32 v40, s28, 0
	s_nop 0
	v_cndmask_b32_e32 v48, 0, v48, vcc
	v_fmaak_f32 v49, v18, v48, 0x4b400000
	v_fmaak_f32 v50, v19, v48, 0x4b400000
	v_fmaak_f32 v51, v20, v48, 0x4b400000
	v_fmaak_f32 v52, v21, v48, 0x4b400000
	v_perm_b32 v49, v50, v49, s33
	v_perm_b32 v51, v52, v51, s34
	v_or_b32_e32 v56, v49, v51
	v_fmaak_f32 v41, v22, v48, 0x4b400000
	v_fmaak_f32 v42, v23, v48, 0x4b400000
	v_fmaak_f32 v43, v24, v48, 0x4b400000
	v_fmaak_f32 v44, v25, v48, 0x4b400000
	v_perm_b32 v41, v42, v41, s33
	v_perm_b32 v43, v44, v43, s34
	v_or_b32_e32 v57, v41, v43
	v_fmaak_f32 v49, v26, v48, 0x4b400000
	v_fmaak_f32 v50, v27, v48, 0x4b400000
	v_fmaak_f32 v51, v28, v48, 0x4b400000
	v_fmaak_f32 v52, v29, v48, 0x4b400000
	v_perm_b32 v49, v50, v49, s33
	v_perm_b32 v51, v52, v51, s34
	v_or_b32_e32 v58, v49, v51
	v_fmaak_f32 v41, v30, v48, 0x4b400000
	v_fmaak_f32 v42, v31, v48, 0x4b400000
	v_fmaak_f32 v43, v32, v48, 0x4b400000
	v_fmaak_f32 v44, v33, v48, 0x4b400000
	v_perm_b32 v41, v42, v41, s33
	v_perm_b32 v43, v44, v43, s34
	v_or_b32_e32 v59, v41, v43
	s_waitcnt vmcnt(0)
	ds_read_b128 v[18:21], v38 offset:0
	ds_read_b128 v[22:25], v38 offset:1024
	ds_read_b128 v[26:29], v38 offset:2048
	ds_read_b128 v[30:33], v38 offset:3072
	s_waitcnt lgkmcnt(0)
	s_barrier
	s_mov_b32 m0, s35
	s_nop 0
	global_load_lds_dwordx4 v34, s[16:17] nt
	global_load_lds_dwordx4 v34, s[16:17] offset:1024 nt
	global_load_lds_dwordx4 v34, s[16:17] offset:2048 nt
	global_load_lds_dwordx4 v35, s[16:17] offset:3072 nt
	s_add_u32 s16, s16, 0xfa0000
	s_addc_u32 s17, s17, 0
	v_cndmask_b32_e64 v30, 0, v30, s[18:19]
	v_cndmask_b32_e64 v31, 0, v31, s[18:19]
	v_cndmask_b32_e64 v32, 0, v32, s[18:19]
	v_cndmask_b32_e64 v33, 0, v33, s[18:19]
	v_max3_f32 v41, |v18|, |v19|, |v20|
	v_max3_f32 v42, |v21|, |v22|, |v23|
	v_max3_f32 v43, |v24|, |v25|, |v26|
	v_max3_f32 v44, |v27|, |v28|, |v29|
	v_max3_f32 v48, |v30|, |v31|, |v32|
	v_max3_f32 v41, v41, v42, |v33|
	v_max3_f32 v43, v43, v44, v48
	v_max_f32_e32 v41, v41, v43
	v_pk_add_f32 v[2:3], v[2:3], v[18:19]
	v_pk_add_f32 v[4:5], v[4:5], v[20:21]
	v_max_f32_dpp v41, v41, v41 quad_perm:[1,0,3,2] row_mask:0xf bank_mask:0xf
	v_pk_add_f32 v[6:7], v[6:7], v[22:23]
	v_pk_add_f32 v[8:9], v[8:9], v[24:25]
	v_max_f32_dpp v41, v41, v41 quad_perm:[2,3,0,1] row_mask:0xf bank_mask:0xf
	v_pk_add_f32 v[10:11], v[10:11], v[26:27]
	v_pk_add_f32 v[12:13], v[12:13], v[28:29]
	v_max_f32_dpp v41, v41, v41 row_half_mirror row_mask:0xf bank_mask:0xf
	v_pk_add_f32 v[14:15], v[14:15], v[30:31]
	v_pk_add_f32 v[16:17], v[16:17], v[32:33]
	v_max_f32_dpp v41, v41, v41 row_mirror row_mask:0xf bank_mask:0xf
	s_nop 1
	v_max_f32_dpp v41, v41, v41 row_bcast:15 row_mask:0xa bank_mask:0xf
	s_nop 1
	v_max_f32_dpp v41, v41, v41 row_bcast:31 row_mask:0xc bank_mask:0xf
	s_nop 1
	v_readlane_b32 s28, v41, 63
	s_nop 1
	v_div_scale_f32 v48, s[30:31], s28, s28, v47
	v_rcp_f32_e32 v49, v48
	s_nop 0
	v_fma_f32 v50, -v48, v49, 1.0
	v_fmac_f32_e32 v49, v50, v49
	v_mov_b32_e32 v50, s28
	v_div_scale_f32 v50, vcc, s32, v50, s32
	v_mul_f32_e32 v51, v50, v49
	v_fma_f32 v52, -v48, v51, v50
	v_fmac_f32_e32 v51, v52, v49
	v_fma_f32 v48, -v48, v51, v50
	v_div_fmas_f32 v48, v48, v49, v51
	v_div_fixup_f32 v48, v48, s28, v47
	v_cmp_gt_f32_e64 vcc, s28, 0
	v_writelane_b32 v40, s28, 1
	s_nop 0
	v_cndmask_b32_e32 v48, 0, v48, vcc
	v_fmaak_f32 v49, v18, v48, 0x4b400000
	v_fmaak_f32 v50, v19, v48, 0x4b400000
	v_fmaak_f32 v51, v20, v48, 0x4b400000
	v_fmaak_f32 v52, v21, v48, 0x4b400000
	v_perm_b32 v49, v50, v49, s33
	v_perm_b32 v51, v52, v51, s34
	v_or_b32_e32 v60, v49, v51
	v_fmaak_f32 v41, v22, v48, 0x4b400000
	v_fmaak_f32 v42, v23, v48, 0x4b400000
	v_fmaak_f32 v43, v24, v48, 0x4b400000
	v_fmaak_f32 v44, v25, v48, 0x4b400000
	v_perm_b32 v41, v42, v41, s33
	v_perm_b32 v43, v44, v43, s34
	v_or_b32_e32 v61, v41, v43
	v_fmaak_f32 v49, v26, v48, 0x4b400000
	v_fmaak_f32 v50, v27, v48, 0x4b400000
	v_fmaak_f32 v51, v28, v48, 0x4b400000
	v_fmaak_f32 v52, v29, v48, 0x4b400000
	v_perm_b32 v49, v50, v49, s33
	v_perm_b32 v51, v52, v51, s34
	v_or_b32_e32 v62, v49, v51
	v_fmaak_f32 v41, v30, v48, 0x4b400000
	v_fmaak_f32 v42, v31, v48, 0x4b400000
	v_fmaak_f32 v43, v32, v48, 0x4b400000
	v_fmaak_f32 v44, v33, v48, 0x4b400000
	v_perm_b32 v41, v42, v41, s33
	v_perm_b32 v43, v44, v43, s34
	v_or_b32_e32 v63, v41, v43
	s_waitcnt vmcnt(0)
	ds_read_b128 v[18:21], v38 offset:0
	ds_read_b128 v[22:25], v38 offset:1024
	ds_read_b128 v[26:29], v38 offset:2048
	ds_read_b128 v[30:33], v38 offset:3072
	s_waitcnt lgkmcnt(0)
	s_barrier
	s_mov_b32 m0, s35
	s_nop 0
	global_load_lds_dwordx4 v34, s[16:17] nt
	global_load_lds_dwordx4 v34, s[16:17] offset:1024 nt
	global_load_lds_dwordx4 v34, s[16:17] offset:2048 nt
	global_load_lds_dwordx4 v35, s[16:17] offset:3072 nt
	s_add_u32 s16, s16, 0xfa0000
	s_addc_u32 s17, s17, 0
	v_cndmask_b32_e64 v30, 0, v30, s[18:19]
	v_cndmask_b32_e64 v31, 0, v31, s[18:19]
	v_cndmask_b32_e64 v32, 0, v32, s[18:19]
	v_cndmask_b32_e64 v33, 0, v33, s[18:19]
	v_max3_f32 v41, |v18|, |v19|, |v20|
	v_max3_f32 v42, |v21|, |v22|, |v23|
	v_max3_f32 v43, |v24|, |v25|, |v26|
	v_max3_f32 v44, |v27|, |v28|, |v29|
	v_max3_f32 v48, |v30|, |v31|, |v32|
	v_max3_f32 v41, v41, v42, |v33|
	v_max3_f32 v43, v43, v44, v48
	v_max_f32_e32 v41, v41, v43
	v_pk_add_f32 v[2:3], v[2:3], v[18:19]
	v_pk_add_f32 v[4:5], v[4:5], v[20:21]
	v_max_f32_dpp v41, v41, v41 quad_perm:[1,0,3,2] row_mask:0xf bank_mask:0xf
	v_pk_add_f32 v[6:7], v[6:7], v[22:23]
	v_pk_add_f32 v[8:9], v[8:9], v[24:25]
	v_max_f32_dpp v41, v41, v41 quad_perm:[2,3,0,1] row_mask:0xf bank_mask:0xf
	v_pk_add_f32 v[10:11], v[10:11], v[26:27]
	v_pk_add_f32 v[12:13], v[12:13], v[28:29]
	v_max_f32_dpp v41, v41, v41 row_half_mirror row_mask:0xf bank_mask:0xf
	v_pk_add_f32 v[14:15], v[14:15], v[30:31]
	v_pk_add_f32 v[16:17], v[16:17], v[32:33]
	v_max_f32_dpp v41, v41, v41 row_mirror row_mask:0xf bank_mask:0xf
	s_nop 1
	v_max_f32_dpp v41, v41, v41 row_bcast:15 row_mask:0xa bank_mask:0xf
	s_nop 1
	v_max_f32_dpp v41, v41, v41 row_bcast:31 row_mask:0xc bank_mask:0xf
	s_nop 1
	v_readlane_b32 s28, v41, 63
	s_nop 1
	v_div_scale_f32 v48, s[30:31], s28, s28, v47
	v_rcp_f32_e32 v49, v48
	s_nop 0
	v_fma_f32 v50, -v48, v49, 1.0
	v_fmac_f32_e32 v49, v50, v49
	v_mov_b32_e32 v50, s28
	v_div_scale_f32 v50, vcc, s32, v50, s32
	v_mul_f32_e32 v51, v50, v49
	v_fma_f32 v52, -v48, v51, v50
	v_fmac_f32_e32 v51, v52, v49
	v_fma_f32 v48, -v48, v51, v50
	v_div_fmas_f32 v48, v48, v49, v51
	v_div_fixup_f32 v48, v48, s28, v47
	v_cmp_gt_f32_e64 vcc, s28, 0
	v_writelane_b32 v40, s28, 2
	s_nop 0
	v_cndmask_b32_e32 v48, 0, v48, vcc
	v_fmaak_f32 v49, v18, v48, 0x4b400000
	v_fmaak_f32 v50, v19, v48, 0x4b400000
	v_fmaak_f32 v51, v20, v48, 0x4b400000
	v_fmaak_f32 v52, v21, v48, 0x4b400000
	v_perm_b32 v49, v50, v49, s33
	v_perm_b32 v51, v52, v51, s34
	v_or_b32_e32 v64, v49, v51
	v_fmaak_f32 v41, v22, v48, 0x4b400000
	v_fmaak_f32 v42, v23, v48, 0x4b400000
	v_fmaak_f32 v43, v24, v48, 0x4b400000
	v_fmaak_f32 v44, v25, v48, 0x4b400000
	v_perm_b32 v41, v42, v41, s33
	v_perm_b32 v43, v44, v43, s34
	v_or_b32_e32 v65, v41, v43
	v_fmaak_f32 v49, v26, v48, 0x4b400000
	v_fmaak_f32 v50, v27, v48, 0x4b400000
	v_fmaak_f32 v51, v28, v48, 0x4b400000
	v_fmaak_f32 v52, v29, v48, 0x4b400000
	v_perm_b32 v49, v50, v49, s33
	v_perm_b32 v51, v52, v51, s34
	v_or_b32_e32 v66, v49, v51
	v_fmaak_f32 v41, v30, v48, 0x4b400000
	v_fmaak_f32 v42, v31, v48, 0x4b400000
	v_fmaak_f32 v43, v32, v48, 0x4b400000
	v_fmaak_f32 v44, v33, v48, 0x4b400000
	v_perm_b32 v41, v42, v41, s33
	v_perm_b32 v43, v44, v43, s34
	v_or_b32_e32 v67, v41, v43
	s_waitcnt vmcnt(0)
	ds_read_b128 v[18:21], v38 offset:0
	ds_read_b128 v[22:25], v38 offset:1024
	ds_read_b128 v[26:29], v38 offset:2048
	ds_read_b128 v[30:33], v38 offset:3072
	s_waitcnt lgkmcnt(0)
	s_barrier
	s_mov_b32 m0, s35
	s_nop 0
	global_load_lds_dwordx4 v34, s[16:17] nt
	global_load_lds_dwordx4 v34, s[16:17] offset:1024 nt
	global_load_lds_dwordx4 v34, s[16:17] offset:2048 nt
	global_load_lds_dwordx4 v35, s[16:17] offset:3072 nt
	s_add_u32 s16, s16, 0xfa0000
	s_addc_u32 s17, s17, 0
	v_cndmask_b32_e64 v30, 0, v30, s[18:19]
	v_cndmask_b32_e64 v31, 0, v31, s[18:19]
	v_cndmask_b32_e64 v32, 0, v32, s[18:19]
	v_cndmask_b32_e64 v33, 0, v33, s[18:19]
	v_max3_f32 v41, |v18|, |v19|, |v20|
	v_max3_f32 v42, |v21|, |v22|, |v23|
	v_max3_f32 v43, |v24|, |v25|, |v26|
	v_max3_f32 v44, |v27|, |v28|, |v29|
	v_max3_f32 v48, |v30|, |v31|, |v32|
	v_max3_f32 v41, v41, v42, |v33|
	v_max3_f32 v43, v43, v44, v48
	v_max_f32_e32 v41, v41, v43
	v_pk_add_f32 v[2:3], v[2:3], v[18:19]
	v_pk_add_f32 v[4:5], v[4:5], v[20:21]
	v_max_f32_dpp v41, v41, v41 quad_perm:[1,0,3,2] row_mask:0xf bank_mask:0xf
	v_pk_add_f32 v[6:7], v[6:7], v[22:23]
	v_pk_add_f32 v[8:9], v[8:9], v[24:25]
	v_max_f32_dpp v41, v41, v41 quad_perm:[2,3,0,1] row_mask:0xf bank_mask:0xf
	v_pk_add_f32 v[10:11], v[10:11], v[26:27]
	v_pk_add_f32 v[12:13], v[12:13], v[28:29]
	v_max_f32_dpp v41, v41, v41 row_half_mirror row_mask:0xf bank_mask:0xf
	v_pk_add_f32 v[14:15], v[14:15], v[30:31]
	v_pk_add_f32 v[16:17], v[16:17], v[32:33]
	v_max_f32_dpp v41, v41, v41 row_mirror row_mask:0xf bank_mask:0xf
	s_nop 1
	v_max_f32_dpp v41, v41, v41 row_bcast:15 row_mask:0xa bank_mask:0xf
	s_nop 1
	v_max_f32_dpp v41, v41, v41 row_bcast:31 row_mask:0xc bank_mask:0xf
	s_nop 1
	v_readlane_b32 s28, v41, 63
	s_nop 1
	v_div_scale_f32 v48, s[30:31], s28, s28, v47
	v_rcp_f32_e32 v49, v48
	s_nop 0
	v_fma_f32 v50, -v48, v49, 1.0
	v_fmac_f32_e32 v49, v50, v49
	v_mov_b32_e32 v50, s28
	v_div_scale_f32 v50, vcc, s32, v50, s32
	v_mul_f32_e32 v51, v50, v49
	v_fma_f32 v52, -v48, v51, v50
	v_fmac_f32_e32 v51, v52, v49
	v_fma_f32 v48, -v48, v51, v50
	v_div_fmas_f32 v48, v48, v49, v51
	v_div_fixup_f32 v48, v48, s28, v47
	v_cmp_gt_f32_e64 vcc, s28, 0
	v_writelane_b32 v40, s28, 3
	s_nop 0
	v_cndmask_b32_e32 v48, 0, v48, vcc
	v_fmaak_f32 v49, v18, v48, 0x4b400000
	v_fmaak_f32 v50, v19, v48, 0x4b400000
	v_fmaak_f32 v51, v20, v48, 0x4b400000
	v_fmaak_f32 v52, v21, v48, 0x4b400000
	v_perm_b32 v49, v50, v49, s33
	v_perm_b32 v51, v52, v51, s34
	v_or_b32_e32 v68, v49, v51
	v_fmaak_f32 v41, v22, v48, 0x4b400000
	v_fmaak_f32 v42, v23, v48, 0x4b400000
	v_fmaak_f32 v43, v24, v48, 0x4b400000
	v_fmaak_f32 v44, v25, v48, 0x4b400000
	v_perm_b32 v41, v42, v41, s33
	v_perm_b32 v43, v44, v43, s34
	v_or_b32_e32 v69, v41, v43
	v_fmaak_f32 v49, v26, v48, 0x4b400000
	v_fmaak_f32 v50, v27, v48, 0x4b400000
	v_fmaak_f32 v51, v28, v48, 0x4b400000
	v_fmaak_f32 v52, v29, v48, 0x4b400000
	v_perm_b32 v49, v50, v49, s33
	v_perm_b32 v51, v52, v51, s34
	v_or_b32_e32 v70, v49, v51
	v_fmaak_f32 v41, v30, v48, 0x4b400000
	v_fmaak_f32 v42, v31, v48, 0x4b400000
	v_fmaak_f32 v43, v32, v48, 0x4b400000
	v_fmaak_f32 v44, v33, v48, 0x4b400000
	v_perm_b32 v41, v42, v41, s33
	v_perm_b32 v43, v44, v43, s34
	v_or_b32_e32 v71, v41, v43
	s_waitcnt vmcnt(0)
	ds_read_b128 v[18:21], v38 offset:0
	ds_read_b128 v[22:25], v38 offset:1024
	ds_read_b128 v[26:29], v38 offset:2048
	ds_read_b128 v[30:33], v38 offset:3072
	s_waitcnt lgkmcnt(0)
	s_barrier
	s_mov_b32 m0, s35
	s_nop 0
	global_load_lds_dwordx4 v34, s[16:17] nt
	global_load_lds_dwordx4 v34, s[16:17] offset:1024 nt
	global_load_lds_dwordx4 v34, s[16:17] offset:2048 nt
	global_load_lds_dwordx4 v35, s[16:17] offset:3072 nt
	s_add_u32 s16, s16, 0xfa0000
	s_addc_u32 s17, s17, 0
	v_cndmask_b32_e64 v30, 0, v30, s[18:19]
	v_cndmask_b32_e64 v31, 0, v31, s[18:19]
	v_cndmask_b32_e64 v32, 0, v32, s[18:19]
	v_cndmask_b32_e64 v33, 0, v33, s[18:19]
	v_max3_f32 v41, |v18|, |v19|, |v20|
	v_max3_f32 v42, |v21|, |v22|, |v23|
	v_max3_f32 v43, |v24|, |v25|, |v26|
	v_max3_f32 v44, |v27|, |v28|, |v29|
	v_max3_f32 v48, |v30|, |v31|, |v32|
	v_max3_f32 v41, v41, v42, |v33|
	v_max3_f32 v43, v43, v44, v48
	v_max_f32_e32 v41, v41, v43
	v_pk_add_f32 v[2:3], v[2:3], v[18:19]
	v_pk_add_f32 v[4:5], v[4:5], v[20:21]
	v_max_f32_dpp v41, v41, v41 quad_perm:[1,0,3,2] row_mask:0xf bank_mask:0xf
	v_pk_add_f32 v[6:7], v[6:7], v[22:23]
	v_pk_add_f32 v[8:9], v[8:9], v[24:25]
	v_max_f32_dpp v41, v41, v41 quad_perm:[2,3,0,1] row_mask:0xf bank_mask:0xf
	v_pk_add_f32 v[10:11], v[10:11], v[26:27]
	v_pk_add_f32 v[12:13], v[12:13], v[28:29]
	v_max_f32_dpp v41, v41, v41 row_half_mirror row_mask:0xf bank_mask:0xf
	v_pk_add_f32 v[14:15], v[14:15], v[30:31]
	v_pk_add_f32 v[16:17], v[16:17], v[32:33]
	v_max_f32_dpp v41, v41, v41 row_mirror row_mask:0xf bank_mask:0xf
	s_nop 1
	v_max_f32_dpp v41, v41, v41 row_bcast:15 row_mask:0xa bank_mask:0xf
	s_nop 1
	v_max_f32_dpp v41, v41, v41 row_bcast:31 row_mask:0xc bank_mask:0xf
	s_nop 1
	v_readlane_b32 s28, v41, 63
	s_nop 1
	v_div_scale_f32 v48, s[30:31], s28, s28, v47
	v_rcp_f32_e32 v49, v48
	s_nop 0
	v_fma_f32 v50, -v48, v49, 1.0
	v_fmac_f32_e32 v49, v50, v49
	v_mov_b32_e32 v50, s28
	v_div_scale_f32 v50, vcc, s32, v50, s32
	v_mul_f32_e32 v51, v50, v49
	v_fma_f32 v52, -v48, v51, v50
	v_fmac_f32_e32 v51, v52, v49
	v_fma_f32 v48, -v48, v51, v50
	v_div_fmas_f32 v48, v48, v49, v51
	v_div_fixup_f32 v48, v48, s28, v47
	v_cmp_gt_f32_e64 vcc, s28, 0
	v_writelane_b32 v40, s28, 4
	s_nop 0
	v_cndmask_b32_e32 v48, 0, v48, vcc
	v_fmaak_f32 v49, v18, v48, 0x4b400000
	v_fmaak_f32 v50, v19, v48, 0x4b400000
	v_fmaak_f32 v51, v20, v48, 0x4b400000
	v_fmaak_f32 v52, v21, v48, 0x4b400000
	v_perm_b32 v49, v50, v49, s33
	v_perm_b32 v51, v52, v51, s34
	v_or_b32_e32 v72, v49, v51
	v_fmaak_f32 v41, v22, v48, 0x4b400000
	v_fmaak_f32 v42, v23, v48, 0x4b400000
	v_fmaak_f32 v43, v24, v48, 0x4b400000
	v_fmaak_f32 v44, v25, v48, 0x4b400000
	v_perm_b32 v41, v42, v41, s33
	v_perm_b32 v43, v44, v43, s34
	v_or_b32_e32 v73, v41, v43
	v_fmaak_f32 v49, v26, v48, 0x4b400000
	v_fmaak_f32 v50, v27, v48, 0x4b400000
	v_fmaak_f32 v51, v28, v48, 0x4b400000
	v_fmaak_f32 v52, v29, v48, 0x4b400000
	v_perm_b32 v49, v50, v49, s33
	v_perm_b32 v51, v52, v51, s34
	v_or_b32_e32 v74, v49, v51
	v_fmaak_f32 v41, v30, v48, 0x4b400000
	v_fmaak_f32 v42, v31, v48, 0x4b400000
	v_fmaak_f32 v43, v32, v48, 0x4b400000
	v_fmaak_f32 v44, v33, v48, 0x4b400000
	v_perm_b32 v41, v42, v41, s33
	v_perm_b32 v43, v44, v43, s34
	v_or_b32_e32 v75, v41, v43
	s_waitcnt vmcnt(0)
	ds_read_b128 v[18:21], v38 offset:0
	ds_read_b128 v[22:25], v38 offset:1024
	ds_read_b128 v[26:29], v38 offset:2048
	ds_read_b128 v[30:33], v38 offset:3072
	s_waitcnt lgkmcnt(0)
	s_barrier
	s_mov_b32 m0, s35
	s_nop 0
	global_load_lds_dwordx4 v34, s[16:17] nt
	global_load_lds_dwordx4 v34, s[16:17] offset:1024 nt
	global_load_lds_dwordx4 v34, s[16:17] offset:2048 nt
	global_load_lds_dwordx4 v35, s[16:17] offset:3072 nt
	s_add_u32 s16, s16, 0xfa0000
	s_addc_u32 s17, s17, 0
	v_cndmask_b32_e64 v30, 0, v30, s[18:19]
	v_cndmask_b32_e64 v31, 0, v31, s[18:19]
	v_cndmask_b32_e64 v32, 0, v32, s[18:19]
	v_cndmask_b32_e64 v33, 0, v33, s[18:19]
	v_max3_f32 v41, |v18|, |v19|, |v20|
	v_max3_f32 v42, |v21|, |v22|, |v23|
	v_max3_f32 v43, |v24|, |v25|, |v26|
	v_max3_f32 v44, |v27|, |v28|, |v29|
	v_max3_f32 v48, |v30|, |v31|, |v32|
	v_max3_f32 v41, v41, v42, |v33|
	v_max3_f32 v43, v43, v44, v48
	v_max_f32_e32 v41, v41, v43
	v_pk_add_f32 v[2:3], v[2:3], v[18:19]
	v_pk_add_f32 v[4:5], v[4:5], v[20:21]
	v_max_f32_dpp v41, v41, v41 quad_perm:[1,0,3,2] row_mask:0xf bank_mask:0xf
	v_pk_add_f32 v[6:7], v[6:7], v[22:23]
	v_pk_add_f32 v[8:9], v[8:9], v[24:25]
	v_max_f32_dpp v41, v41, v41 quad_perm:[2,3,0,1] row_mask:0xf bank_mask:0xf
	v_pk_add_f32 v[10:11], v[10:11], v[26:27]
	v_pk_add_f32 v[12:13], v[12:13], v[28:29]
	v_max_f32_dpp v41, v41, v41 row_half_mirror row_mask:0xf bank_mask:0xf
	v_pk_add_f32 v[14:15], v[14:15], v[30:31]
	v_pk_add_f32 v[16:17], v[16:17], v[32:33]
	v_max_f32_dpp v41, v41, v41 row_mirror row_mask:0xf bank_mask:0xf
	s_nop 1
	v_max_f32_dpp v41, v41, v41 row_bcast:15 row_mask:0xa bank_mask:0xf
	s_nop 1
	v_max_f32_dpp v41, v41, v41 row_bcast:31 row_mask:0xc bank_mask:0xf
	s_nop 1
	v_readlane_b32 s28, v41, 63
	s_nop 1
	v_div_scale_f32 v48, s[30:31], s28, s28, v47
	v_rcp_f32_e32 v49, v48
	s_nop 0
	v_fma_f32 v50, -v48, v49, 1.0
	v_fmac_f32_e32 v49, v50, v49
	v_mov_b32_e32 v50, s28
	v_div_scale_f32 v50, vcc, s32, v50, s32
	v_mul_f32_e32 v51, v50, v49
	v_fma_f32 v52, -v48, v51, v50
	v_fmac_f32_e32 v51, v52, v49
	v_fma_f32 v48, -v48, v51, v50
	v_div_fmas_f32 v48, v48, v49, v51
	v_div_fixup_f32 v48, v48, s28, v47
	v_cmp_gt_f32_e64 vcc, s28, 0
	v_writelane_b32 v40, s28, 5
	s_nop 0
	v_cndmask_b32_e32 v48, 0, v48, vcc
	v_fmaak_f32 v49, v18, v48, 0x4b400000
	v_fmaak_f32 v50, v19, v48, 0x4b400000
	v_fmaak_f32 v51, v20, v48, 0x4b400000
	v_fmaak_f32 v52, v21, v48, 0x4b400000
	v_perm_b32 v49, v50, v49, s33
	v_perm_b32 v51, v52, v51, s34
	v_or_b32_e32 v76, v49, v51
	v_fmaak_f32 v41, v22, v48, 0x4b400000
	v_fmaak_f32 v42, v23, v48, 0x4b400000
	v_fmaak_f32 v43, v24, v48, 0x4b400000
	v_fmaak_f32 v44, v25, v48, 0x4b400000
	v_perm_b32 v41, v42, v41, s33
	v_perm_b32 v43, v44, v43, s34
	v_or_b32_e32 v77, v41, v43
	v_fmaak_f32 v49, v26, v48, 0x4b400000
	v_fmaak_f32 v50, v27, v48, 0x4b400000
	v_fmaak_f32 v51, v28, v48, 0x4b400000
	v_fmaak_f32 v52, v29, v48, 0x4b400000
	v_perm_b32 v49, v50, v49, s33
	v_perm_b32 v51, v52, v51, s34
	v_or_b32_e32 v78, v49, v51
	v_fmaak_f32 v41, v30, v48, 0x4b400000
	v_fmaak_f32 v42, v31, v48, 0x4b400000
	v_fmaak_f32 v43, v32, v48, 0x4b400000
	v_fmaak_f32 v44, v33, v48, 0x4b400000
	v_perm_b32 v41, v42, v41, s33
	v_perm_b32 v43, v44, v43, s34
	v_or_b32_e32 v79, v41, v43
	s_waitcnt vmcnt(0)
	ds_read_b128 v[18:21], v38 offset:0
	ds_read_b128 v[22:25], v38 offset:1024
	ds_read_b128 v[26:29], v38 offset:2048
	ds_read_b128 v[30:33], v38 offset:3072
	s_waitcnt lgkmcnt(0)
	s_barrier
	s_mov_b32 m0, s35
	s_nop 0
	global_load_lds_dwordx4 v34, s[16:17] nt
	global_load_lds_dwordx4 v34, s[16:17] offset:1024 nt
	global_load_lds_dwordx4 v34, s[16:17] offset:2048 nt
	global_load_lds_dwordx4 v35, s[16:17] offset:3072 nt
	s_add_u32 s16, s16, 0xfa0000
	s_addc_u32 s17, s17, 0
	v_cndmask_b32_e64 v30, 0, v30, s[18:19]
	v_cndmask_b32_e64 v31, 0, v31, s[18:19]
	v_cndmask_b32_e64 v32, 0, v32, s[18:19]
	v_cndmask_b32_e64 v33, 0, v33, s[18:19]
	v_max3_f32 v41, |v18|, |v19|, |v20|
	v_max3_f32 v42, |v21|, |v22|, |v23|
	v_max3_f32 v43, |v24|, |v25|, |v26|
	v_max3_f32 v44, |v27|, |v28|, |v29|
	v_max3_f32 v48, |v30|, |v31|, |v32|
	v_max3_f32 v41, v41, v42, |v33|
	v_max3_f32 v43, v43, v44, v48
	v_max_f32_e32 v41, v41, v43
	v_pk_add_f32 v[2:3], v[2:3], v[18:19]
	v_pk_add_f32 v[4:5], v[4:5], v[20:21]
	v_max_f32_dpp v41, v41, v41 quad_perm:[1,0,3,2] row_mask:0xf bank_mask:0xf
	v_pk_add_f32 v[6:7], v[6:7], v[22:23]
	v_pk_add_f32 v[8:9], v[8:9], v[24:25]
	v_max_f32_dpp v41, v41, v41 quad_perm:[2,3,0,1] row_mask:0xf bank_mask:0xf
	v_pk_add_f32 v[10:11], v[10:11], v[26:27]
	v_pk_add_f32 v[12:13], v[12:13], v[28:29]
	v_max_f32_dpp v41, v41, v41 row_half_mirror row_mask:0xf bank_mask:0xf
	v_pk_add_f32 v[14:15], v[14:15], v[30:31]
	v_pk_add_f32 v[16:17], v[16:17], v[32:33]
	v_max_f32_dpp v41, v41, v41 row_mirror row_mask:0xf bank_mask:0xf
	s_nop 1
	v_max_f32_dpp v41, v41, v41 row_bcast:15 row_mask:0xa bank_mask:0xf
	s_nop 1
	v_max_f32_dpp v41, v41, v41 row_bcast:31 row_mask:0xc bank_mask:0xf
	s_nop 1
	v_readlane_b32 s28, v41, 63
	s_nop 1
	v_div_scale_f32 v48, s[30:31], s28, s28, v47
	v_rcp_f32_e32 v49, v48
	s_nop 0
	v_fma_f32 v50, -v48, v49, 1.0
	v_fmac_f32_e32 v49, v50, v49
	v_mov_b32_e32 v50, s28
	v_div_scale_f32 v50, vcc, s32, v50, s32
	v_mul_f32_e32 v51, v50, v49
	v_fma_f32 v52, -v48, v51, v50
	v_fmac_f32_e32 v51, v52, v49
	v_fma_f32 v48, -v48, v51, v50
	v_div_fmas_f32 v48, v48, v49, v51
	v_div_fixup_f32 v48, v48, s28, v47
	v_cmp_gt_f32_e64 vcc, s28, 0
	v_writelane_b32 v40, s28, 6
	s_nop 0
	v_cndmask_b32_e32 v48, 0, v48, vcc
	v_fmaak_f32 v49, v18, v48, 0x4b400000
	v_fmaak_f32 v50, v19, v48, 0x4b400000
	v_fmaak_f32 v51, v20, v48, 0x4b400000
	v_fmaak_f32 v52, v21, v48, 0x4b400000
	v_perm_b32 v49, v50, v49, s33
	v_perm_b32 v51, v52, v51, s34
	v_or_b32_e32 v80, v49, v51
	v_fmaak_f32 v41, v22, v48, 0x4b400000
	v_fmaak_f32 v42, v23, v48, 0x4b400000
	v_fmaak_f32 v43, v24, v48, 0x4b400000
	v_fmaak_f32 v44, v25, v48, 0x4b400000
	v_perm_b32 v41, v42, v41, s33
	v_perm_b32 v43, v44, v43, s34
	v_or_b32_e32 v81, v41, v43
	v_fmaak_f32 v49, v26, v48, 0x4b400000
	v_fmaak_f32 v50, v27, v48, 0x4b400000
	v_fmaak_f32 v51, v28, v48, 0x4b400000
	v_fmaak_f32 v52, v29, v48, 0x4b400000
	v_perm_b32 v49, v50, v49, s33
	v_perm_b32 v51, v52, v51, s34
	v_or_b32_e32 v82, v49, v51
	v_fmaak_f32 v41, v30, v48, 0x4b400000
	v_fmaak_f32 v42, v31, v48, 0x4b400000
	v_fmaak_f32 v43, v32, v48, 0x4b400000
	v_fmaak_f32 v44, v33, v48, 0x4b400000
	v_perm_b32 v41, v42, v41, s33
	v_perm_b32 v43, v44, v43, s34
	v_or_b32_e32 v83, v41, v43
	s_waitcnt vmcnt(0)
	ds_read_b128 v[18:21], v38 offset:0
	ds_read_b128 v[22:25], v38 offset:1024
	ds_read_b128 v[26:29], v38 offset:2048
	ds_read_b128 v[30:33], v38 offset:3072
	s_waitcnt lgkmcnt(0)
	s_barrier
	s_mov_b32 m0, s35
	s_nop 0
	global_load_lds_dwordx4 v34, s[16:17] nt
	global_load_lds_dwordx4 v34, s[16:17] offset:1024 nt
	global_load_lds_dwordx4 v34, s[16:17] offset:2048 nt
	global_load_lds_dwordx4 v35, s[16:17] offset:3072 nt
	s_add_u32 s16, s16, 0xfa0000
	s_addc_u32 s17, s17, 0
	v_cndmask_b32_e64 v30, 0, v30, s[18:19]
	v_cndmask_b32_e64 v31, 0, v31, s[18:19]
	v_cndmask_b32_e64 v32, 0, v32, s[18:19]
	v_cndmask_b32_e64 v33, 0, v33, s[18:19]
	v_max3_f32 v41, |v18|, |v19|, |v20|
	v_max3_f32 v42, |v21|, |v22|, |v23|
	v_max3_f32 v43, |v24|, |v25|, |v26|
	v_max3_f32 v44, |v27|, |v28|, |v29|
	v_max3_f32 v48, |v30|, |v31|, |v32|
	v_max3_f32 v41, v41, v42, |v33|
	v_max3_f32 v43, v43, v44, v48
	v_max_f32_e32 v41, v41, v43
	v_pk_add_f32 v[2:3], v[2:3], v[18:19]
	v_pk_add_f32 v[4:5], v[4:5], v[20:21]
	v_max_f32_dpp v41, v41, v41 quad_perm:[1,0,3,2] row_mask:0xf bank_mask:0xf
	v_pk_add_f32 v[6:7], v[6:7], v[22:23]
	v_pk_add_f32 v[8:9], v[8:9], v[24:25]
	v_max_f32_dpp v41, v41, v41 quad_perm:[2,3,0,1] row_mask:0xf bank_mask:0xf
	v_pk_add_f32 v[10:11], v[10:11], v[26:27]
	v_pk_add_f32 v[12:13], v[12:13], v[28:29]
	v_max_f32_dpp v41, v41, v41 row_half_mirror row_mask:0xf bank_mask:0xf
	v_pk_add_f32 v[14:15], v[14:15], v[30:31]
	v_pk_add_f32 v[16:17], v[16:17], v[32:33]
	v_max_f32_dpp v41, v41, v41 row_mirror row_mask:0xf bank_mask:0xf
	s_nop 1
	v_max_f32_dpp v41, v41, v41 row_bcast:15 row_mask:0xa bank_mask:0xf
	s_nop 1
	v_max_f32_dpp v41, v41, v41 row_bcast:31 row_mask:0xc bank_mask:0xf
	s_nop 1
	v_readlane_b32 s28, v41, 63
	s_nop 1
	v_div_scale_f32 v48, s[30:31], s28, s28, v47
	v_rcp_f32_e32 v49, v48
	s_nop 0
	v_fma_f32 v50, -v48, v49, 1.0
	v_fmac_f32_e32 v49, v50, v49
	v_mov_b32_e32 v50, s28
	v_div_scale_f32 v50, vcc, s32, v50, s32
	v_mul_f32_e32 v51, v50, v49
	v_fma_f32 v52, -v48, v51, v50
	v_fmac_f32_e32 v51, v52, v49
	v_fma_f32 v48, -v48, v51, v50
	v_div_fmas_f32 v48, v48, v49, v51
	v_div_fixup_f32 v48, v48, s28, v47
	v_cmp_gt_f32_e64 vcc, s28, 0
	v_writelane_b32 v40, s28, 7
	s_nop 0
	v_cndmask_b32_e32 v48, 0, v48, vcc
	v_fmaak_f32 v49, v18, v48, 0x4b400000
	v_fmaak_f32 v50, v19, v48, 0x4b400000
	v_fmaak_f32 v51, v20, v48, 0x4b400000
	v_fmaak_f32 v52, v21, v48, 0x4b400000
	v_perm_b32 v49, v50, v49, s33
	v_perm_b32 v51, v52, v51, s34
	v_or_b32_e32 v84, v49, v51
	v_fmaak_f32 v41, v22, v48, 0x4b400000
	v_fmaak_f32 v42, v23, v48, 0x4b400000
	v_fmaak_f32 v43, v24, v48, 0x4b400000
	v_fmaak_f32 v44, v25, v48, 0x4b400000
	v_perm_b32 v41, v42, v41, s33
	v_perm_b32 v43, v44, v43, s34
	v_or_b32_e32 v85, v41, v43
	v_fmaak_f32 v49, v26, v48, 0x4b400000
	v_fmaak_f32 v50, v27, v48, 0x4b400000
	v_fmaak_f32 v51, v28, v48, 0x4b400000
	v_fmaak_f32 v52, v29, v48, 0x4b400000
	v_perm_b32 v49, v50, v49, s33
	v_perm_b32 v51, v52, v51, s34
	v_or_b32_e32 v86, v49, v51
	v_fmaak_f32 v41, v30, v48, 0x4b400000
	v_fmaak_f32 v42, v31, v48, 0x4b400000
	v_fmaak_f32 v43, v32, v48, 0x4b400000
	v_fmaak_f32 v44, v33, v48, 0x4b400000
	v_perm_b32 v41, v42, v41, s33
	v_perm_b32 v43, v44, v43, s34
	v_or_b32_e32 v87, v41, v43
	s_waitcnt vmcnt(0)
	ds_read_b128 v[18:21], v38 offset:0
	ds_read_b128 v[22:25], v38 offset:1024
	ds_read_b128 v[26:29], v38 offset:2048
	ds_read_b128 v[30:33], v38 offset:3072
	s_waitcnt lgkmcnt(0)
	s_barrier
	s_mov_b32 m0, s35
	s_nop 0
	global_load_lds_dwordx4 v34, s[16:17] nt
	global_load_lds_dwordx4 v34, s[16:17] offset:1024 nt
	global_load_lds_dwordx4 v34, s[16:17] offset:2048 nt
	global_load_lds_dwordx4 v35, s[16:17] offset:3072 nt
	s_add_u32 s16, s16, 0xfa0000
	s_addc_u32 s17, s17, 0
	v_cndmask_b32_e64 v30, 0, v30, s[18:19]
	v_cndmask_b32_e64 v31, 0, v31, s[18:19]
	v_cndmask_b32_e64 v32, 0, v32, s[18:19]
	v_cndmask_b32_e64 v33, 0, v33, s[18:19]
	v_max3_f32 v41, |v18|, |v19|, |v20|
	v_max3_f32 v42, |v21|, |v22|, |v23|
	v_max3_f32 v43, |v24|, |v25|, |v26|
	v_max3_f32 v44, |v27|, |v28|, |v29|
	v_max3_f32 v48, |v30|, |v31|, |v32|
	v_max3_f32 v41, v41, v42, |v33|
	v_max3_f32 v43, v43, v44, v48
	v_max_f32_e32 v41, v41, v43
	v_pk_add_f32 v[2:3], v[2:3], v[18:19]
	v_pk_add_f32 v[4:5], v[4:5], v[20:21]
	v_max_f32_dpp v41, v41, v41 quad_perm:[1,0,3,2] row_mask:0xf bank_mask:0xf
	v_pk_add_f32 v[6:7], v[6:7], v[22:23]
	v_pk_add_f32 v[8:9], v[8:9], v[24:25]
	v_max_f32_dpp v41, v41, v41 quad_perm:[2,3,0,1] row_mask:0xf bank_mask:0xf
	v_pk_add_f32 v[10:11], v[10:11], v[26:27]
	v_pk_add_f32 v[12:13], v[12:13], v[28:29]
	v_max_f32_dpp v41, v41, v41 row_half_mirror row_mask:0xf bank_mask:0xf
	v_pk_add_f32 v[14:15], v[14:15], v[30:31]
	v_pk_add_f32 v[16:17], v[16:17], v[32:33]
	v_max_f32_dpp v41, v41, v41 row_mirror row_mask:0xf bank_mask:0xf
	s_nop 1
	v_max_f32_dpp v41, v41, v41 row_bcast:15 row_mask:0xa bank_mask:0xf
	s_nop 1
	v_max_f32_dpp v41, v41, v41 row_bcast:31 row_mask:0xc bank_mask:0xf
	s_nop 1
	v_readlane_b32 s28, v41, 63
	s_nop 1
	v_div_scale_f32 v48, s[30:31], s28, s28, v47
	v_rcp_f32_e32 v49, v48
	s_nop 0
	v_fma_f32 v50, -v48, v49, 1.0
	v_fmac_f32_e32 v49, v50, v49
	v_mov_b32_e32 v50, s28
	v_div_scale_f32 v50, vcc, s32, v50, s32
	v_mul_f32_e32 v51, v50, v49
	v_fma_f32 v52, -v48, v51, v50
	v_fmac_f32_e32 v51, v52, v49
	v_fma_f32 v48, -v48, v51, v50
	v_div_fmas_f32 v48, v48, v49, v51
	v_div_fixup_f32 v48, v48, s28, v47
	v_cmp_gt_f32_e64 vcc, s28, 0
	v_writelane_b32 v40, s28, 8
	s_nop 0
	v_cndmask_b32_e32 v48, 0, v48, vcc
	v_fmaak_f32 v49, v18, v48, 0x4b400000
	v_fmaak_f32 v50, v19, v48, 0x4b400000
	v_fmaak_f32 v51, v20, v48, 0x4b400000
	v_fmaak_f32 v52, v21, v48, 0x4b400000
	v_perm_b32 v49, v50, v49, s33
	v_perm_b32 v51, v52, v51, s34
	v_or_b32_e32 v88, v49, v51
	v_fmaak_f32 v41, v22, v48, 0x4b400000
	v_fmaak_f32 v42, v23, v48, 0x4b400000
	v_fmaak_f32 v43, v24, v48, 0x4b400000
	v_fmaak_f32 v44, v25, v48, 0x4b400000
	v_perm_b32 v41, v42, v41, s33
	v_perm_b32 v43, v44, v43, s34
	v_or_b32_e32 v89, v41, v43
	v_fmaak_f32 v49, v26, v48, 0x4b400000
	v_fmaak_f32 v50, v27, v48, 0x4b400000
	v_fmaak_f32 v51, v28, v48, 0x4b400000
	v_fmaak_f32 v52, v29, v48, 0x4b400000
	v_perm_b32 v49, v50, v49, s33
	v_perm_b32 v51, v52, v51, s34
	v_or_b32_e32 v90, v49, v51
	v_fmaak_f32 v41, v30, v48, 0x4b400000
	v_fmaak_f32 v42, v31, v48, 0x4b400000
	v_fmaak_f32 v43, v32, v48, 0x4b400000
	v_fmaak_f32 v44, v33, v48, 0x4b400000
	v_perm_b32 v41, v42, v41, s33
	v_perm_b32 v43, v44, v43, s34
	v_or_b32_e32 v91, v41, v43
	s_waitcnt vmcnt(0)
	ds_read_b128 v[18:21], v38 offset:0
	ds_read_b128 v[22:25], v38 offset:1024
	ds_read_b128 v[26:29], v38 offset:2048
	ds_read_b128 v[30:33], v38 offset:3072
	s_waitcnt lgkmcnt(0)
	s_barrier
	s_mov_b32 m0, s35
	s_nop 0
	global_load_lds_dwordx4 v34, s[16:17] nt
	global_load_lds_dwordx4 v34, s[16:17] offset:1024 nt
	global_load_lds_dwordx4 v34, s[16:17] offset:2048 nt
	global_load_lds_dwordx4 v35, s[16:17] offset:3072 nt
	s_add_u32 s16, s16, 0xfa0000
	s_addc_u32 s17, s17, 0
	v_cndmask_b32_e64 v30, 0, v30, s[18:19]
	v_cndmask_b32_e64 v31, 0, v31, s[18:19]
	v_cndmask_b32_e64 v32, 0, v32, s[18:19]
	v_cndmask_b32_e64 v33, 0, v33, s[18:19]
	v_max3_f32 v41, |v18|, |v19|, |v20|
	v_max3_f32 v42, |v21|, |v22|, |v23|
	v_max3_f32 v43, |v24|, |v25|, |v26|
	v_max3_f32 v44, |v27|, |v28|, |v29|
	v_max3_f32 v48, |v30|, |v31|, |v32|
	v_max3_f32 v41, v41, v42, |v33|
	v_max3_f32 v43, v43, v44, v48
	v_max_f32_e32 v41, v41, v43
	v_pk_add_f32 v[2:3], v[2:3], v[18:19]
	v_pk_add_f32 v[4:5], v[4:5], v[20:21]
	v_max_f32_dpp v41, v41, v41 quad_perm:[1,0,3,2] row_mask:0xf bank_mask:0xf
	v_pk_add_f32 v[6:7], v[6:7], v[22:23]
	v_pk_add_f32 v[8:9], v[8:9], v[24:25]
	v_max_f32_dpp v41, v41, v41 quad_perm:[2,3,0,1] row_mask:0xf bank_mask:0xf
	v_pk_add_f32 v[10:11], v[10:11], v[26:27]
	v_pk_add_f32 v[12:13], v[12:13], v[28:29]
	v_max_f32_dpp v41, v41, v41 row_half_mirror row_mask:0xf bank_mask:0xf
	v_pk_add_f32 v[14:15], v[14:15], v[30:31]
	v_pk_add_f32 v[16:17], v[16:17], v[32:33]
	v_max_f32_dpp v41, v41, v41 row_mirror row_mask:0xf bank_mask:0xf
	s_nop 1
	v_max_f32_dpp v41, v41, v41 row_bcast:15 row_mask:0xa bank_mask:0xf
	s_nop 1
	v_max_f32_dpp v41, v41, v41 row_bcast:31 row_mask:0xc bank_mask:0xf
	s_nop 1
	v_readlane_b32 s28, v41, 63
	s_nop 1
	v_div_scale_f32 v48, s[30:31], s28, s28, v47
	v_rcp_f32_e32 v49, v48
	s_nop 0
	v_fma_f32 v50, -v48, v49, 1.0
	v_fmac_f32_e32 v49, v50, v49
	v_mov_b32_e32 v50, s28
	v_div_scale_f32 v50, vcc, s32, v50, s32
	v_mul_f32_e32 v51, v50, v49
	v_fma_f32 v52, -v48, v51, v50
	v_fmac_f32_e32 v51, v52, v49
	v_fma_f32 v48, -v48, v51, v50
	v_div_fmas_f32 v48, v48, v49, v51
	v_div_fixup_f32 v48, v48, s28, v47
	v_cmp_gt_f32_e64 vcc, s28, 0
	v_writelane_b32 v40, s28, 9
	s_nop 0
	v_cndmask_b32_e32 v48, 0, v48, vcc
	v_fmaak_f32 v49, v18, v48, 0x4b400000
	v_fmaak_f32 v50, v19, v48, 0x4b400000
	v_fmaak_f32 v51, v20, v48, 0x4b400000
	v_fmaak_f32 v52, v21, v48, 0x4b400000
	v_perm_b32 v49, v50, v49, s33
	v_perm_b32 v51, v52, v51, s34
	v_or_b32_e32 v92, v49, v51
	v_fmaak_f32 v41, v22, v48, 0x4b400000
	v_fmaak_f32 v42, v23, v48, 0x4b400000
	v_fmaak_f32 v43, v24, v48, 0x4b400000
	v_fmaak_f32 v44, v25, v48, 0x4b400000
	v_perm_b32 v41, v42, v41, s33
	v_perm_b32 v43, v44, v43, s34
	v_or_b32_e32 v93, v41, v43
	v_fmaak_f32 v49, v26, v48, 0x4b400000
	v_fmaak_f32 v50, v27, v48, 0x4b400000
	v_fmaak_f32 v51, v28, v48, 0x4b400000
	v_fmaak_f32 v52, v29, v48, 0x4b400000
	v_perm_b32 v49, v50, v49, s33
	v_perm_b32 v51, v52, v51, s34
	v_or_b32_e32 v94, v49, v51
	v_fmaak_f32 v41, v30, v48, 0x4b400000
	v_fmaak_f32 v42, v31, v48, 0x4b400000
	v_fmaak_f32 v43, v32, v48, 0x4b400000
	v_fmaak_f32 v44, v33, v48, 0x4b400000
	v_perm_b32 v41, v42, v41, s33
	v_perm_b32 v43, v44, v43, s34
	v_or_b32_e32 v95, v41, v43
	s_waitcnt vmcnt(0)
	ds_read_b128 v[18:21], v38 offset:0
	ds_read_b128 v[22:25], v38 offset:1024
	ds_read_b128 v[26:29], v38 offset:2048
	ds_read_b128 v[30:33], v38 offset:3072
	s_waitcnt lgkmcnt(0)
	s_barrier
	s_mov_b32 m0, s35
	s_nop 0
	global_load_lds_dwordx4 v34, s[16:17] nt
	global_load_lds_dwordx4 v34, s[16:17] offset:1024 nt
	global_load_lds_dwordx4 v34, s[16:17] offset:2048 nt
	global_load_lds_dwordx4 v35, s[16:17] offset:3072 nt
	s_add_u32 s16, s16, 0xfa0000
	s_addc_u32 s17, s17, 0
	v_cndmask_b32_e64 v30, 0, v30, s[18:19]
	v_cndmask_b32_e64 v31, 0, v31, s[18:19]
	v_cndmask_b32_e64 v32, 0, v32, s[18:19]
	v_cndmask_b32_e64 v33, 0, v33, s[18:19]
	v_max3_f32 v41, |v18|, |v19|, |v20|
	v_max3_f32 v42, |v21|, |v22|, |v23|
	v_max3_f32 v43, |v24|, |v25|, |v26|
	v_max3_f32 v44, |v27|, |v28|, |v29|
	v_max3_f32 v48, |v30|, |v31|, |v32|
	v_max3_f32 v41, v41, v42, |v33|
	v_max3_f32 v43, v43, v44, v48
	v_max_f32_e32 v41, v41, v43
	v_pk_add_f32 v[2:3], v[2:3], v[18:19]
	v_pk_add_f32 v[4:5], v[4:5], v[20:21]
	v_max_f32_dpp v41, v41, v41 quad_perm:[1,0,3,2] row_mask:0xf bank_mask:0xf
	v_pk_add_f32 v[6:7], v[6:7], v[22:23]
	v_pk_add_f32 v[8:9], v[8:9], v[24:25]
	v_max_f32_dpp v41, v41, v41 quad_perm:[2,3,0,1] row_mask:0xf bank_mask:0xf
	v_pk_add_f32 v[10:11], v[10:11], v[26:27]
	v_pk_add_f32 v[12:13], v[12:13], v[28:29]
	v_max_f32_dpp v41, v41, v41 row_half_mirror row_mask:0xf bank_mask:0xf
	v_pk_add_f32 v[14:15], v[14:15], v[30:31]
	v_pk_add_f32 v[16:17], v[16:17], v[32:33]
	v_max_f32_dpp v41, v41, v41 row_mirror row_mask:0xf bank_mask:0xf
	s_nop 1
	v_max_f32_dpp v41, v41, v41 row_bcast:15 row_mask:0xa bank_mask:0xf
	s_nop 1
	v_max_f32_dpp v41, v41, v41 row_bcast:31 row_mask:0xc bank_mask:0xf
	s_nop 1
	v_readlane_b32 s28, v41, 63
	s_nop 1
	v_div_scale_f32 v48, s[30:31], s28, s28, v47
	v_rcp_f32_e32 v49, v48
	s_nop 0
	v_fma_f32 v50, -v48, v49, 1.0
	v_fmac_f32_e32 v49, v50, v49
	v_mov_b32_e32 v50, s28
	v_div_scale_f32 v50, vcc, s32, v50, s32
	v_mul_f32_e32 v51, v50, v49
	v_fma_f32 v52, -v48, v51, v50
	v_fmac_f32_e32 v51, v52, v49
	v_fma_f32 v48, -v48, v51, v50
	v_div_fmas_f32 v48, v48, v49, v51
	v_div_fixup_f32 v48, v48, s28, v47
	v_cmp_gt_f32_e64 vcc, s28, 0
	v_writelane_b32 v40, s28, 10
	s_nop 0
	v_cndmask_b32_e32 v48, 0, v48, vcc
	v_fmaak_f32 v49, v18, v48, 0x4b400000
	v_fmaak_f32 v50, v19, v48, 0x4b400000
	v_fmaak_f32 v51, v20, v48, 0x4b400000
	v_fmaak_f32 v52, v21, v48, 0x4b400000
	v_perm_b32 v49, v50, v49, s33
	v_perm_b32 v51, v52, v51, s34
	v_or_b32_e32 v96, v49, v51
	v_fmaak_f32 v41, v22, v48, 0x4b400000
	v_fmaak_f32 v42, v23, v48, 0x4b400000
	v_fmaak_f32 v43, v24, v48, 0x4b400000
	v_fmaak_f32 v44, v25, v48, 0x4b400000
	v_perm_b32 v41, v42, v41, s33
	v_perm_b32 v43, v44, v43, s34
	v_or_b32_e32 v97, v41, v43
	v_fmaak_f32 v49, v26, v48, 0x4b400000
	v_fmaak_f32 v50, v27, v48, 0x4b400000
	v_fmaak_f32 v51, v28, v48, 0x4b400000
	v_fmaak_f32 v52, v29, v48, 0x4b400000
	v_perm_b32 v49, v50, v49, s33
	v_perm_b32 v51, v52, v51, s34
	v_or_b32_e32 v98, v49, v51
	v_fmaak_f32 v41, v30, v48, 0x4b400000
	v_fmaak_f32 v42, v31, v48, 0x4b400000
	v_fmaak_f32 v43, v32, v48, 0x4b400000
	v_fmaak_f32 v44, v33, v48, 0x4b400000
	v_perm_b32 v41, v42, v41, s33
	v_perm_b32 v43, v44, v43, s34
	v_or_b32_e32 v99, v41, v43
	s_waitcnt vmcnt(0)
	ds_read_b128 v[18:21], v38 offset:0
	ds_read_b128 v[22:25], v38 offset:1024
	ds_read_b128 v[26:29], v38 offset:2048
	ds_read_b128 v[30:33], v38 offset:3072
	s_waitcnt lgkmcnt(0)
	s_barrier
	s_mov_b32 m0, s35
	s_nop 0
	global_load_lds_dwordx4 v34, s[16:17] nt
	global_load_lds_dwordx4 v34, s[16:17] offset:1024 nt
	global_load_lds_dwordx4 v34, s[16:17] offset:2048 nt
	global_load_lds_dwordx4 v35, s[16:17] offset:3072 nt
	s_add_u32 s16, s16, 0xfa0000
	s_addc_u32 s17, s17, 0
	v_cndmask_b32_e64 v30, 0, v30, s[18:19]
	v_cndmask_b32_e64 v31, 0, v31, s[18:19]
	v_cndmask_b32_e64 v32, 0, v32, s[18:19]
	v_cndmask_b32_e64 v33, 0, v33, s[18:19]
	v_max3_f32 v41, |v18|, |v19|, |v20|
	v_max3_f32 v42, |v21|, |v22|, |v23|
	v_max3_f32 v43, |v24|, |v25|, |v26|
	v_max3_f32 v44, |v27|, |v28|, |v29|
	v_max3_f32 v48, |v30|, |v31|, |v32|
	v_max3_f32 v41, v41, v42, |v33|
	v_max3_f32 v43, v43, v44, v48
	v_max_f32_e32 v41, v41, v43
	v_pk_add_f32 v[2:3], v[2:3], v[18:19]
	v_pk_add_f32 v[4:5], v[4:5], v[20:21]
	v_max_f32_dpp v41, v41, v41 quad_perm:[1,0,3,2] row_mask:0xf bank_mask:0xf
	v_pk_add_f32 v[6:7], v[6:7], v[22:23]
	v_pk_add_f32 v[8:9], v[8:9], v[24:25]
	v_max_f32_dpp v41, v41, v41 quad_perm:[2,3,0,1] row_mask:0xf bank_mask:0xf
	v_pk_add_f32 v[10:11], v[10:11], v[26:27]
	v_pk_add_f32 v[12:13], v[12:13], v[28:29]
	v_max_f32_dpp v41, v41, v41 row_half_mirror row_mask:0xf bank_mask:0xf
	v_pk_add_f32 v[14:15], v[14:15], v[30:31]
	v_pk_add_f32 v[16:17], v[16:17], v[32:33]
	v_max_f32_dpp v41, v41, v41 row_mirror row_mask:0xf bank_mask:0xf
	s_nop 1
	v_max_f32_dpp v41, v41, v41 row_bcast:15 row_mask:0xa bank_mask:0xf
	s_nop 1
	v_max_f32_dpp v41, v41, v41 row_bcast:31 row_mask:0xc bank_mask:0xf
	s_nop 1
	v_readlane_b32 s28, v41, 63
	s_nop 1
	v_div_scale_f32 v48, s[30:31], s28, s28, v47
	v_rcp_f32_e32 v49, v48
	s_nop 0
	v_fma_f32 v50, -v48, v49, 1.0
	v_fmac_f32_e32 v49, v50, v49
	v_mov_b32_e32 v50, s28
	v_div_scale_f32 v50, vcc, s32, v50, s32
	v_mul_f32_e32 v51, v50, v49
	v_fma_f32 v52, -v48, v51, v50
	v_fmac_f32_e32 v51, v52, v49
	v_fma_f32 v48, -v48, v51, v50
	v_div_fmas_f32 v48, v48, v49, v51
	v_div_fixup_f32 v48, v48, s28, v47
	v_cmp_gt_f32_e64 vcc, s28, 0
	v_writelane_b32 v40, s28, 11
	s_nop 0
	v_cndmask_b32_e32 v48, 0, v48, vcc
	v_fmaak_f32 v49, v18, v48, 0x4b400000
	v_fmaak_f32 v50, v19, v48, 0x4b400000
	v_fmaak_f32 v51, v20, v48, 0x4b400000
	v_fmaak_f32 v52, v21, v48, 0x4b400000
	v_perm_b32 v49, v50, v49, s33
	v_perm_b32 v51, v52, v51, s34
	v_or_b32_e32 v100, v49, v51
	v_fmaak_f32 v41, v22, v48, 0x4b400000
	v_fmaak_f32 v42, v23, v48, 0x4b400000
	v_fmaak_f32 v43, v24, v48, 0x4b400000
	v_fmaak_f32 v44, v25, v48, 0x4b400000
	v_perm_b32 v41, v42, v41, s33
	v_perm_b32 v43, v44, v43, s34
	v_or_b32_e32 v101, v41, v43
	v_fmaak_f32 v49, v26, v48, 0x4b400000
	v_fmaak_f32 v50, v27, v48, 0x4b400000
	v_fmaak_f32 v51, v28, v48, 0x4b400000
	v_fmaak_f32 v52, v29, v48, 0x4b400000
	v_perm_b32 v49, v50, v49, s33
	v_perm_b32 v51, v52, v51, s34
	v_or_b32_e32 v102, v49, v51
	v_fmaak_f32 v41, v30, v48, 0x4b400000
	v_fmaak_f32 v42, v31, v48, 0x4b400000
	v_fmaak_f32 v43, v32, v48, 0x4b400000
	v_fmaak_f32 v44, v33, v48, 0x4b400000
	v_perm_b32 v41, v42, v41, s33
	v_perm_b32 v43, v44, v43, s34
	v_or_b32_e32 v103, v41, v43
	s_waitcnt vmcnt(0)
	ds_read_b128 v[18:21], v38 offset:0
	ds_read_b128 v[22:25], v38 offset:1024
	ds_read_b128 v[26:29], v38 offset:2048
	ds_read_b128 v[30:33], v38 offset:3072
	s_waitcnt lgkmcnt(0)
	s_barrier
	s_mov_b32 m0, s35
	s_nop 0
	global_load_lds_dwordx4 v34, s[16:17] nt
	global_load_lds_dwordx4 v34, s[16:17] offset:1024 nt
	global_load_lds_dwordx4 v34, s[16:17] offset:2048 nt
	global_load_lds_dwordx4 v35, s[16:17] offset:3072 nt
	s_add_u32 s16, s16, 0xfa0000
	s_addc_u32 s17, s17, 0
	v_cndmask_b32_e64 v30, 0, v30, s[18:19]
	v_cndmask_b32_e64 v31, 0, v31, s[18:19]
	v_cndmask_b32_e64 v32, 0, v32, s[18:19]
	v_cndmask_b32_e64 v33, 0, v33, s[18:19]
	v_max3_f32 v41, |v18|, |v19|, |v20|
	v_max3_f32 v42, |v21|, |v22|, |v23|
	v_max3_f32 v43, |v24|, |v25|, |v26|
	v_max3_f32 v44, |v27|, |v28|, |v29|
	v_max3_f32 v48, |v30|, |v31|, |v32|
	v_max3_f32 v41, v41, v42, |v33|
	v_max3_f32 v43, v43, v44, v48
	v_max_f32_e32 v41, v41, v43
	v_pk_add_f32 v[2:3], v[2:3], v[18:19]
	v_pk_add_f32 v[4:5], v[4:5], v[20:21]
	v_max_f32_dpp v41, v41, v41 quad_perm:[1,0,3,2] row_mask:0xf bank_mask:0xf
	v_pk_add_f32 v[6:7], v[6:7], v[22:23]
	v_pk_add_f32 v[8:9], v[8:9], v[24:25]
	v_max_f32_dpp v41, v41, v41 quad_perm:[2,3,0,1] row_mask:0xf bank_mask:0xf
	v_pk_add_f32 v[10:11], v[10:11], v[26:27]
	v_pk_add_f32 v[12:13], v[12:13], v[28:29]
	v_max_f32_dpp v41, v41, v41 row_half_mirror row_mask:0xf bank_mask:0xf
	v_pk_add_f32 v[14:15], v[14:15], v[30:31]
	v_pk_add_f32 v[16:17], v[16:17], v[32:33]
	v_max_f32_dpp v41, v41, v41 row_mirror row_mask:0xf bank_mask:0xf
	s_nop 1
	v_max_f32_dpp v41, v41, v41 row_bcast:15 row_mask:0xa bank_mask:0xf
	s_nop 1
	v_max_f32_dpp v41, v41, v41 row_bcast:31 row_mask:0xc bank_mask:0xf
	s_nop 1
	v_readlane_b32 s28, v41, 63
	s_nop 1
	v_div_scale_f32 v48, s[30:31], s28, s28, v47
	v_rcp_f32_e32 v49, v48
	s_nop 0
	v_fma_f32 v50, -v48, v49, 1.0
	v_fmac_f32_e32 v49, v50, v49
	v_mov_b32_e32 v50, s28
	v_div_scale_f32 v50, vcc, s32, v50, s32
	v_mul_f32_e32 v51, v50, v49
	v_fma_f32 v52, -v48, v51, v50
	v_fmac_f32_e32 v51, v52, v49
	v_fma_f32 v48, -v48, v51, v50
	v_div_fmas_f32 v48, v48, v49, v51
	v_div_fixup_f32 v48, v48, s28, v47
	v_cmp_gt_f32_e64 vcc, s28, 0
	v_writelane_b32 v40, s28, 12
	s_nop 0
	v_cndmask_b32_e32 v48, 0, v48, vcc
	v_fmaak_f32 v49, v18, v48, 0x4b400000
	v_fmaak_f32 v50, v19, v48, 0x4b400000
	v_fmaak_f32 v51, v20, v48, 0x4b400000
	v_fmaak_f32 v52, v21, v48, 0x4b400000
	v_perm_b32 v49, v50, v49, s33
	v_perm_b32 v51, v52, v51, s34
	v_or_b32_e32 v104, v49, v51
	v_fmaak_f32 v41, v22, v48, 0x4b400000
	v_fmaak_f32 v42, v23, v48, 0x4b400000
	v_fmaak_f32 v43, v24, v48, 0x4b400000
	v_fmaak_f32 v44, v25, v48, 0x4b400000
	v_perm_b32 v41, v42, v41, s33
	v_perm_b32 v43, v44, v43, s34
	v_or_b32_e32 v105, v41, v43
	v_fmaak_f32 v49, v26, v48, 0x4b400000
	v_fmaak_f32 v50, v27, v48, 0x4b400000
	v_fmaak_f32 v51, v28, v48, 0x4b400000
	v_fmaak_f32 v52, v29, v48, 0x4b400000
	v_perm_b32 v49, v50, v49, s33
	v_perm_b32 v51, v52, v51, s34
	v_or_b32_e32 v106, v49, v51
	v_fmaak_f32 v41, v30, v48, 0x4b400000
	v_fmaak_f32 v42, v31, v48, 0x4b400000
	v_fmaak_f32 v43, v32, v48, 0x4b400000
	v_fmaak_f32 v44, v33, v48, 0x4b400000
	v_perm_b32 v41, v42, v41, s33
	v_perm_b32 v43, v44, v43, s34
	v_or_b32_e32 v107, v41, v43
	s_waitcnt vmcnt(0)
	ds_read_b128 v[18:21], v38 offset:0
	ds_read_b128 v[22:25], v38 offset:1024
	ds_read_b128 v[26:29], v38 offset:2048
	ds_read_b128 v[30:33], v38 offset:3072
	s_waitcnt lgkmcnt(0)
	s_barrier
	s_mov_b32 m0, s35
	s_nop 0
	global_load_lds_dwordx4 v34, s[16:17] nt
	global_load_lds_dwordx4 v34, s[16:17] offset:1024 nt
	global_load_lds_dwordx4 v34, s[16:17] offset:2048 nt
	global_load_lds_dwordx4 v35, s[16:17] offset:3072 nt
	s_add_u32 s16, s16, 0xfa0000
	s_addc_u32 s17, s17, 0
	v_cndmask_b32_e64 v30, 0, v30, s[18:19]
	v_cndmask_b32_e64 v31, 0, v31, s[18:19]
	v_cndmask_b32_e64 v32, 0, v32, s[18:19]
	v_cndmask_b32_e64 v33, 0, v33, s[18:19]
	v_max3_f32 v41, |v18|, |v19|, |v20|
	v_max3_f32 v42, |v21|, |v22|, |v23|
	v_max3_f32 v43, |v24|, |v25|, |v26|
	v_max3_f32 v44, |v27|, |v28|, |v29|
	v_max3_f32 v48, |v30|, |v31|, |v32|
	v_max3_f32 v41, v41, v42, |v33|
	v_max3_f32 v43, v43, v44, v48
	v_max_f32_e32 v41, v41, v43
	v_pk_add_f32 v[2:3], v[2:3], v[18:19]
	v_pk_add_f32 v[4:5], v[4:5], v[20:21]
	v_max_f32_dpp v41, v41, v41 quad_perm:[1,0,3,2] row_mask:0xf bank_mask:0xf
	v_pk_add_f32 v[6:7], v[6:7], v[22:23]
	v_pk_add_f32 v[8:9], v[8:9], v[24:25]
	v_max_f32_dpp v41, v41, v41 quad_perm:[2,3,0,1] row_mask:0xf bank_mask:0xf
	v_pk_add_f32 v[10:11], v[10:11], v[26:27]
	v_pk_add_f32 v[12:13], v[12:13], v[28:29]
	v_max_f32_dpp v41, v41, v41 row_half_mirror row_mask:0xf bank_mask:0xf
	v_pk_add_f32 v[14:15], v[14:15], v[30:31]
	v_pk_add_f32 v[16:17], v[16:17], v[32:33]
	v_max_f32_dpp v41, v41, v41 row_mirror row_mask:0xf bank_mask:0xf
	s_nop 1
	v_max_f32_dpp v41, v41, v41 row_bcast:15 row_mask:0xa bank_mask:0xf
	s_nop 1
	v_max_f32_dpp v41, v41, v41 row_bcast:31 row_mask:0xc bank_mask:0xf
	s_nop 1
	v_readlane_b32 s28, v41, 63
	s_nop 1
	v_div_scale_f32 v48, s[30:31], s28, s28, v47
	v_rcp_f32_e32 v49, v48
	s_nop 0
	v_fma_f32 v50, -v48, v49, 1.0
	v_fmac_f32_e32 v49, v50, v49
	v_mov_b32_e32 v50, s28
	v_div_scale_f32 v50, vcc, s32, v50, s32
	v_mul_f32_e32 v51, v50, v49
	v_fma_f32 v52, -v48, v51, v50
	v_fmac_f32_e32 v51, v52, v49
	v_fma_f32 v48, -v48, v51, v50
	v_div_fmas_f32 v48, v48, v49, v51
	v_div_fixup_f32 v48, v48, s28, v47
	v_cmp_gt_f32_e64 vcc, s28, 0
	v_writelane_b32 v40, s28, 13
	s_nop 0
	v_cndmask_b32_e32 v48, 0, v48, vcc
	v_fmaak_f32 v49, v18, v48, 0x4b400000
	v_fmaak_f32 v50, v19, v48, 0x4b400000
	v_fmaak_f32 v51, v20, v48, 0x4b400000
	v_fmaak_f32 v52, v21, v48, 0x4b400000
	v_perm_b32 v49, v50, v49, s33
	v_perm_b32 v51, v52, v51, s34
	v_or_b32_e32 v108, v49, v51
	v_fmaak_f32 v41, v22, v48, 0x4b400000
	v_fmaak_f32 v42, v23, v48, 0x4b400000
	v_fmaak_f32 v43, v24, v48, 0x4b400000
	v_fmaak_f32 v44, v25, v48, 0x4b400000
	v_perm_b32 v41, v42, v41, s33
	v_perm_b32 v43, v44, v43, s34
	v_or_b32_e32 v109, v41, v43
	v_fmaak_f32 v49, v26, v48, 0x4b400000
	v_fmaak_f32 v50, v27, v48, 0x4b400000
	v_fmaak_f32 v51, v28, v48, 0x4b400000
	v_fmaak_f32 v52, v29, v48, 0x4b400000
	v_perm_b32 v49, v50, v49, s33
	v_perm_b32 v51, v52, v51, s34
	v_or_b32_e32 v110, v49, v51
	v_fmaak_f32 v41, v30, v48, 0x4b400000
	v_fmaak_f32 v42, v31, v48, 0x4b400000
	v_fmaak_f32 v43, v32, v48, 0x4b400000
	v_fmaak_f32 v44, v33, v48, 0x4b400000
	v_perm_b32 v41, v42, v41, s33
	v_perm_b32 v43, v44, v43, s34
	v_or_b32_e32 v111, v41, v43
	s_waitcnt vmcnt(0)
	ds_read_b128 v[18:21], v38 offset:0
	ds_read_b128 v[22:25], v38 offset:1024
	ds_read_b128 v[26:29], v38 offset:2048
	ds_read_b128 v[30:33], v38 offset:3072
	s_waitcnt lgkmcnt(0)
	s_barrier
	s_mov_b32 m0, s35
	s_nop 0
	global_load_lds_dwordx4 v34, s[16:17] nt
	global_load_lds_dwordx4 v34, s[16:17] offset:1024 nt
	global_load_lds_dwordx4 v34, s[16:17] offset:2048 nt
	global_load_lds_dwordx4 v35, s[16:17] offset:3072 nt
	s_add_u32 s16, s16, 0xfa0000
	s_addc_u32 s17, s17, 0
	v_cndmask_b32_e64 v30, 0, v30, s[18:19]
	v_cndmask_b32_e64 v31, 0, v31, s[18:19]
	v_cndmask_b32_e64 v32, 0, v32, s[18:19]
	v_cndmask_b32_e64 v33, 0, v33, s[18:19]
	v_max3_f32 v41, |v18|, |v19|, |v20|
	v_max3_f32 v42, |v21|, |v22|, |v23|
	v_max3_f32 v43, |v24|, |v25|, |v26|
	v_max3_f32 v44, |v27|, |v28|, |v29|
	v_max3_f32 v48, |v30|, |v31|, |v32|
	v_max3_f32 v41, v41, v42, |v33|
	v_max3_f32 v43, v43, v44, v48
	v_max_f32_e32 v41, v41, v43
	v_pk_add_f32 v[2:3], v[2:3], v[18:19]
	v_pk_add_f32 v[4:5], v[4:5], v[20:21]
	v_max_f32_dpp v41, v41, v41 quad_perm:[1,0,3,2] row_mask:0xf bank_mask:0xf
	v_pk_add_f32 v[6:7], v[6:7], v[22:23]
	v_pk_add_f32 v[8:9], v[8:9], v[24:25]
	v_max_f32_dpp v41, v41, v41 quad_perm:[2,3,0,1] row_mask:0xf bank_mask:0xf
	v_pk_add_f32 v[10:11], v[10:11], v[26:27]
	v_pk_add_f32 v[12:13], v[12:13], v[28:29]
	v_max_f32_dpp v41, v41, v41 row_half_mirror row_mask:0xf bank_mask:0xf
	v_pk_add_f32 v[14:15], v[14:15], v[30:31]
	v_pk_add_f32 v[16:17], v[16:17], v[32:33]
	v_max_f32_dpp v41, v41, v41 row_mirror row_mask:0xf bank_mask:0xf
	s_nop 1
	v_max_f32_dpp v41, v41, v41 row_bcast:15 row_mask:0xa bank_mask:0xf
	s_nop 1
	v_max_f32_dpp v41, v41, v41 row_bcast:31 row_mask:0xc bank_mask:0xf
	s_nop 1
	v_readlane_b32 s28, v41, 63
	s_nop 1
	v_div_scale_f32 v48, s[30:31], s28, s28, v47
	v_rcp_f32_e32 v49, v48
	s_nop 0
	v_fma_f32 v50, -v48, v49, 1.0
	v_fmac_f32_e32 v49, v50, v49
	v_mov_b32_e32 v50, s28
	v_div_scale_f32 v50, vcc, s32, v50, s32
	v_mul_f32_e32 v51, v50, v49
	v_fma_f32 v52, -v48, v51, v50
	v_fmac_f32_e32 v51, v52, v49
	v_fma_f32 v48, -v48, v51, v50
	v_div_fmas_f32 v48, v48, v49, v51
	v_div_fixup_f32 v48, v48, s28, v47
	v_cmp_gt_f32_e64 vcc, s28, 0
	v_writelane_b32 v40, s28, 14
	s_nop 0
	v_cndmask_b32_e32 v48, 0, v48, vcc
	v_fmaak_f32 v49, v18, v48, 0x4b400000
	v_fmaak_f32 v50, v19, v48, 0x4b400000
	v_fmaak_f32 v51, v20, v48, 0x4b400000
	v_fmaak_f32 v52, v21, v48, 0x4b400000
	v_perm_b32 v49, v50, v49, s33
	v_perm_b32 v51, v52, v51, s34
	v_or_b32_e32 v112, v49, v51
	v_fmaak_f32 v41, v22, v48, 0x4b400000
	v_fmaak_f32 v42, v23, v48, 0x4b400000
	v_fmaak_f32 v43, v24, v48, 0x4b400000
	v_fmaak_f32 v44, v25, v48, 0x4b400000
	v_perm_b32 v41, v42, v41, s33
	v_perm_b32 v43, v44, v43, s34
	v_or_b32_e32 v113, v41, v43
	v_fmaak_f32 v49, v26, v48, 0x4b400000
	v_fmaak_f32 v50, v27, v48, 0x4b400000
	v_fmaak_f32 v51, v28, v48, 0x4b400000
	v_fmaak_f32 v52, v29, v48, 0x4b400000
	v_perm_b32 v49, v50, v49, s33
	v_perm_b32 v51, v52, v51, s34
	v_or_b32_e32 v114, v49, v51
	v_fmaak_f32 v41, v30, v48, 0x4b400000
	v_fmaak_f32 v42, v31, v48, 0x4b400000
	v_fmaak_f32 v43, v32, v48, 0x4b400000
	v_fmaak_f32 v44, v33, v48, 0x4b400000
	v_perm_b32 v41, v42, v41, s33
	v_perm_b32 v43, v44, v43, s34
	v_or_b32_e32 v115, v41, v43
	s_waitcnt vmcnt(0)
	ds_read_b128 v[18:21], v38 offset:0
	ds_read_b128 v[22:25], v38 offset:1024
	ds_read_b128 v[26:29], v38 offset:2048
	ds_read_b128 v[30:33], v38 offset:3072
	s_waitcnt lgkmcnt(0)
	s_barrier
	s_mov_b32 m0, s35
	s_nop 0
	global_load_lds_dwordx4 v34, s[16:17] nt
	global_load_lds_dwordx4 v34, s[16:17] offset:1024 nt
	global_load_lds_dwordx4 v34, s[16:17] offset:2048 nt
	global_load_lds_dwordx4 v35, s[16:17] offset:3072 nt
	s_add_u32 s16, s16, 0xfa0000
	s_addc_u32 s17, s17, 0
	v_cndmask_b32_e64 v30, 0, v30, s[18:19]
	v_cndmask_b32_e64 v31, 0, v31, s[18:19]
	v_cndmask_b32_e64 v32, 0, v32, s[18:19]
	v_cndmask_b32_e64 v33, 0, v33, s[18:19]
	v_max3_f32 v41, |v18|, |v19|, |v20|
	v_max3_f32 v42, |v21|, |v22|, |v23|
	v_max3_f32 v43, |v24|, |v25|, |v26|
	v_max3_f32 v44, |v27|, |v28|, |v29|
	v_max3_f32 v48, |v30|, |v31|, |v32|
	v_max3_f32 v41, v41, v42, |v33|
	v_max3_f32 v43, v43, v44, v48
	v_max_f32_e32 v41, v41, v43
	v_pk_add_f32 v[2:3], v[2:3], v[18:19]
	v_pk_add_f32 v[4:5], v[4:5], v[20:21]
	v_max_f32_dpp v41, v41, v41 quad_perm:[1,0,3,2] row_mask:0xf bank_mask:0xf
	v_pk_add_f32 v[6:7], v[6:7], v[22:23]
	v_pk_add_f32 v[8:9], v[8:9], v[24:25]
	v_max_f32_dpp v41, v41, v41 quad_perm:[2,3,0,1] row_mask:0xf bank_mask:0xf
	v_pk_add_f32 v[10:11], v[10:11], v[26:27]
	v_pk_add_f32 v[12:13], v[12:13], v[28:29]
	v_max_f32_dpp v41, v41, v41 row_half_mirror row_mask:0xf bank_mask:0xf
	v_pk_add_f32 v[14:15], v[14:15], v[30:31]
	v_pk_add_f32 v[16:17], v[16:17], v[32:33]
	v_max_f32_dpp v41, v41, v41 row_mirror row_mask:0xf bank_mask:0xf
	s_nop 1
	v_max_f32_dpp v41, v41, v41 row_bcast:15 row_mask:0xa bank_mask:0xf
	s_nop 1
	v_max_f32_dpp v41, v41, v41 row_bcast:31 row_mask:0xc bank_mask:0xf
	s_nop 1
	v_readlane_b32 s28, v41, 63
	s_nop 1
	v_div_scale_f32 v48, s[30:31], s28, s28, v47
	v_rcp_f32_e32 v49, v48
	s_nop 0
	v_fma_f32 v50, -v48, v49, 1.0
	v_fmac_f32_e32 v49, v50, v49
	v_mov_b32_e32 v50, s28
	v_div_scale_f32 v50, vcc, s32, v50, s32
	v_mul_f32_e32 v51, v50, v49
	v_fma_f32 v52, -v48, v51, v50
	v_fmac_f32_e32 v51, v52, v49
	v_fma_f32 v48, -v48, v51, v50
	v_div_fmas_f32 v48, v48, v49, v51
	v_div_fixup_f32 v48, v48, s28, v47
	v_cmp_gt_f32_e64 vcc, s28, 0
	v_writelane_b32 v40, s28, 15
	s_nop 0
	v_cndmask_b32_e32 v48, 0, v48, vcc
	v_fmaak_f32 v49, v18, v48, 0x4b400000
	v_fmaak_f32 v50, v19, v48, 0x4b400000
	v_fmaak_f32 v51, v20, v48, 0x4b400000
	v_fmaak_f32 v52, v21, v48, 0x4b400000
	v_perm_b32 v49, v50, v49, s33
	v_perm_b32 v51, v52, v51, s34
	v_or_b32_e32 v116, v49, v51
	v_fmaak_f32 v41, v22, v48, 0x4b400000
	v_fmaak_f32 v42, v23, v48, 0x4b400000
	v_fmaak_f32 v43, v24, v48, 0x4b400000
	v_fmaak_f32 v44, v25, v48, 0x4b400000
	v_perm_b32 v41, v42, v41, s33
	v_perm_b32 v43, v44, v43, s34
	v_or_b32_e32 v117, v41, v43
	v_fmaak_f32 v49, v26, v48, 0x4b400000
	v_fmaak_f32 v50, v27, v48, 0x4b400000
	v_fmaak_f32 v51, v28, v48, 0x4b400000
	v_fmaak_f32 v52, v29, v48, 0x4b400000
	v_perm_b32 v49, v50, v49, s33
	v_perm_b32 v51, v52, v51, s34
	v_or_b32_e32 v118, v49, v51
	v_fmaak_f32 v41, v30, v48, 0x4b400000
	v_fmaak_f32 v42, v31, v48, 0x4b400000
	v_fmaak_f32 v43, v32, v48, 0x4b400000
	v_fmaak_f32 v44, v33, v48, 0x4b400000
	v_perm_b32 v41, v42, v41, s33
	v_perm_b32 v43, v44, v43, s34
	v_or_b32_e32 v119, v41, v43
	s_waitcnt vmcnt(0)
	ds_read_b128 v[18:21], v38 offset:0
	ds_read_b128 v[22:25], v38 offset:1024
	ds_read_b128 v[26:29], v38 offset:2048
	ds_read_b128 v[30:33], v38 offset:3072
	s_waitcnt lgkmcnt(0)
	s_barrier
	s_mov_b32 m0, s35
	s_nop 0
	global_load_lds_dwordx4 v34, s[16:17] nt
	global_load_lds_dwordx4 v34, s[16:17] offset:1024 nt
	global_load_lds_dwordx4 v34, s[16:17] offset:2048 nt
	global_load_lds_dwordx4 v35, s[16:17] offset:3072 nt
	s_add_u32 s16, s16, 0xfa0000
	s_addc_u32 s17, s17, 0
	v_cndmask_b32_e64 v30, 0, v30, s[18:19]
	v_cndmask_b32_e64 v31, 0, v31, s[18:19]
	v_cndmask_b32_e64 v32, 0, v32, s[18:19]
	v_cndmask_b32_e64 v33, 0, v33, s[18:19]
	v_max3_f32 v41, |v18|, |v19|, |v20|
	v_max3_f32 v42, |v21|, |v22|, |v23|
	v_max3_f32 v43, |v24|, |v25|, |v26|
	v_max3_f32 v44, |v27|, |v28|, |v29|
	v_max3_f32 v48, |v30|, |v31|, |v32|
	v_max3_f32 v41, v41, v42, |v33|
	v_max3_f32 v43, v43, v44, v48
	v_max_f32_e32 v41, v41, v43
	v_pk_add_f32 v[2:3], v[2:3], v[18:19]
	v_pk_add_f32 v[4:5], v[4:5], v[20:21]
	v_max_f32_dpp v41, v41, v41 quad_perm:[1,0,3,2] row_mask:0xf bank_mask:0xf
	v_pk_add_f32 v[6:7], v[6:7], v[22:23]
	v_pk_add_f32 v[8:9], v[8:9], v[24:25]
	v_max_f32_dpp v41, v41, v41 quad_perm:[2,3,0,1] row_mask:0xf bank_mask:0xf
	v_pk_add_f32 v[10:11], v[10:11], v[26:27]
	v_pk_add_f32 v[12:13], v[12:13], v[28:29]
	v_max_f32_dpp v41, v41, v41 row_half_mirror row_mask:0xf bank_mask:0xf
	v_pk_add_f32 v[14:15], v[14:15], v[30:31]
	v_pk_add_f32 v[16:17], v[16:17], v[32:33]
	v_max_f32_dpp v41, v41, v41 row_mirror row_mask:0xf bank_mask:0xf
	s_nop 1
	v_max_f32_dpp v41, v41, v41 row_bcast:15 row_mask:0xa bank_mask:0xf
	s_nop 1
	v_max_f32_dpp v41, v41, v41 row_bcast:31 row_mask:0xc bank_mask:0xf
	s_nop 1
	v_readlane_b32 s28, v41, 63
	s_nop 1
	v_div_scale_f32 v48, s[30:31], s28, s28, v47
	v_rcp_f32_e32 v49, v48
	s_nop 0
	v_fma_f32 v50, -v48, v49, 1.0
	v_fmac_f32_e32 v49, v50, v49
	v_mov_b32_e32 v50, s28
	v_div_scale_f32 v50, vcc, s32, v50, s32
	v_mul_f32_e32 v51, v50, v49
	v_fma_f32 v52, -v48, v51, v50
	v_fmac_f32_e32 v51, v52, v49
	v_fma_f32 v48, -v48, v51, v50
	v_div_fmas_f32 v48, v48, v49, v51
	v_div_fixup_f32 v48, v48, s28, v47
	v_cmp_gt_f32_e64 vcc, s28, 0
	v_writelane_b32 v40, s28, 16
	s_nop 0
	v_cndmask_b32_e32 v48, 0, v48, vcc
	v_fmaak_f32 v49, v18, v48, 0x4b400000
	v_fmaak_f32 v50, v19, v48, 0x4b400000
	v_fmaak_f32 v51, v20, v48, 0x4b400000
	v_fmaak_f32 v52, v21, v48, 0x4b400000
	v_perm_b32 v49, v50, v49, s33
	v_perm_b32 v51, v52, v51, s34
	v_or_b32_e32 v120, v49, v51
	v_fmaak_f32 v41, v22, v48, 0x4b400000
	v_fmaak_f32 v42, v23, v48, 0x4b400000
	v_fmaak_f32 v43, v24, v48, 0x4b400000
	v_fmaak_f32 v44, v25, v48, 0x4b400000
	v_perm_b32 v41, v42, v41, s33
	v_perm_b32 v43, v44, v43, s34
	v_or_b32_e32 v121, v41, v43
	v_fmaak_f32 v49, v26, v48, 0x4b400000
	v_fmaak_f32 v50, v27, v48, 0x4b400000
	v_fmaak_f32 v51, v28, v48, 0x4b400000
	v_fmaak_f32 v52, v29, v48, 0x4b400000
	v_perm_b32 v49, v50, v49, s33
	v_perm_b32 v51, v52, v51, s34
	v_or_b32_e32 v122, v49, v51
	v_fmaak_f32 v41, v30, v48, 0x4b400000
	v_fmaak_f32 v42, v31, v48, 0x4b400000
	v_fmaak_f32 v43, v32, v48, 0x4b400000
	v_fmaak_f32 v44, v33, v48, 0x4b400000
	v_perm_b32 v41, v42, v41, s33
	v_perm_b32 v43, v44, v43, s34
	v_or_b32_e32 v123, v41, v43
	s_waitcnt vmcnt(0)
	ds_read_b128 v[18:21], v38 offset:0
	ds_read_b128 v[22:25], v38 offset:1024
	ds_read_b128 v[26:29], v38 offset:2048
	ds_read_b128 v[30:33], v38 offset:3072
	s_waitcnt lgkmcnt(0)
	s_barrier
	s_mov_b32 m0, s35
	s_nop 0
	global_load_lds_dwordx4 v34, s[16:17] nt
	global_load_lds_dwordx4 v34, s[16:17] offset:1024 nt
	global_load_lds_dwordx4 v34, s[16:17] offset:2048 nt
	global_load_lds_dwordx4 v35, s[16:17] offset:3072 nt
	s_add_u32 s16, s16, 0xfa0000
	s_addc_u32 s17, s17, 0
	v_cndmask_b32_e64 v30, 0, v30, s[18:19]
	v_cndmask_b32_e64 v31, 0, v31, s[18:19]
	v_cndmask_b32_e64 v32, 0, v32, s[18:19]
	v_cndmask_b32_e64 v33, 0, v33, s[18:19]
	v_max3_f32 v41, |v18|, |v19|, |v20|
	v_max3_f32 v42, |v21|, |v22|, |v23|
	v_max3_f32 v43, |v24|, |v25|, |v26|
	v_max3_f32 v44, |v27|, |v28|, |v29|
	v_max3_f32 v48, |v30|, |v31|, |v32|
	v_max3_f32 v41, v41, v42, |v33|
	v_max3_f32 v43, v43, v44, v48
	v_max_f32_e32 v41, v41, v43
	v_pk_add_f32 v[2:3], v[2:3], v[18:19]
	v_pk_add_f32 v[4:5], v[4:5], v[20:21]
	v_max_f32_dpp v41, v41, v41 quad_perm:[1,0,3,2] row_mask:0xf bank_mask:0xf
	v_pk_add_f32 v[6:7], v[6:7], v[22:23]
	v_pk_add_f32 v[8:9], v[8:9], v[24:25]
	v_max_f32_dpp v41, v41, v41 quad_perm:[2,3,0,1] row_mask:0xf bank_mask:0xf
	v_pk_add_f32 v[10:11], v[10:11], v[26:27]
	v_pk_add_f32 v[12:13], v[12:13], v[28:29]
	v_max_f32_dpp v41, v41, v41 row_half_mirror row_mask:0xf bank_mask:0xf
	v_pk_add_f32 v[14:15], v[14:15], v[30:31]
	v_pk_add_f32 v[16:17], v[16:17], v[32:33]
	v_max_f32_dpp v41, v41, v41 row_mirror row_mask:0xf bank_mask:0xf
	s_nop 1
	v_max_f32_dpp v41, v41, v41 row_bcast:15 row_mask:0xa bank_mask:0xf
	s_nop 1
	v_max_f32_dpp v41, v41, v41 row_bcast:31 row_mask:0xc bank_mask:0xf
	s_nop 1
	v_readlane_b32 s28, v41, 63
	s_nop 1
	v_div_scale_f32 v48, s[30:31], s28, s28, v47
	v_rcp_f32_e32 v49, v48
	s_nop 0
	v_fma_f32 v50, -v48, v49, 1.0
	v_fmac_f32_e32 v49, v50, v49
	v_mov_b32_e32 v50, s28
	v_div_scale_f32 v50, vcc, s32, v50, s32
	v_mul_f32_e32 v51, v50, v49
	v_fma_f32 v52, -v48, v51, v50
	v_fmac_f32_e32 v51, v52, v49
	v_fma_f32 v48, -v48, v51, v50
	v_div_fmas_f32 v48, v48, v49, v51
	v_div_fixup_f32 v48, v48, s28, v47
	v_cmp_gt_f32_e64 vcc, s28, 0
	v_writelane_b32 v40, s28, 17
	s_nop 0
	v_cndmask_b32_e32 v48, 0, v48, vcc
	v_fmaak_f32 v49, v18, v48, 0x4b400000
	v_fmaak_f32 v50, v19, v48, 0x4b400000
	v_fmaak_f32 v51, v20, v48, 0x4b400000
	v_fmaak_f32 v52, v21, v48, 0x4b400000
	v_perm_b32 v49, v50, v49, s33
	v_perm_b32 v51, v52, v51, s34
	v_or_b32_e32 v124, v49, v51
	v_fmaak_f32 v41, v22, v48, 0x4b400000
	v_fmaak_f32 v42, v23, v48, 0x4b400000
	v_fmaak_f32 v43, v24, v48, 0x4b400000
	v_fmaak_f32 v44, v25, v48, 0x4b400000
	v_perm_b32 v41, v42, v41, s33
	v_perm_b32 v43, v44, v43, s34
	v_or_b32_e32 v125, v41, v43
	v_fmaak_f32 v49, v26, v48, 0x4b400000
	v_fmaak_f32 v50, v27, v48, 0x4b400000
	v_fmaak_f32 v51, v28, v48, 0x4b400000
	v_fmaak_f32 v52, v29, v48, 0x4b400000
	v_perm_b32 v49, v50, v49, s33
	v_perm_b32 v51, v52, v51, s34
	v_or_b32_e32 v126, v49, v51
	v_fmaak_f32 v41, v30, v48, 0x4b400000
	v_fmaak_f32 v42, v31, v48, 0x4b400000
	v_fmaak_f32 v43, v32, v48, 0x4b400000
	v_fmaak_f32 v44, v33, v48, 0x4b400000
	v_perm_b32 v41, v42, v41, s33
	v_perm_b32 v43, v44, v43, s34
	v_or_b32_e32 v127, v41, v43
	s_waitcnt vmcnt(0)
	ds_read_b128 v[18:21], v38 offset:0
	ds_read_b128 v[22:25], v38 offset:1024
	ds_read_b128 v[26:29], v38 offset:2048
	ds_read_b128 v[30:33], v38 offset:3072
	s_waitcnt lgkmcnt(0)
	s_barrier
	s_mov_b32 m0, s35
	s_nop 0
	global_load_lds_dwordx4 v34, s[16:17] nt
	global_load_lds_dwordx4 v34, s[16:17] offset:1024 nt
	global_load_lds_dwordx4 v34, s[16:17] offset:2048 nt
	global_load_lds_dwordx4 v35, s[16:17] offset:3072 nt
	s_add_u32 s16, s16, 0xfa0000
	s_addc_u32 s17, s17, 0
	v_cndmask_b32_e64 v30, 0, v30, s[18:19]
	v_cndmask_b32_e64 v31, 0, v31, s[18:19]
	v_cndmask_b32_e64 v32, 0, v32, s[18:19]
	v_cndmask_b32_e64 v33, 0, v33, s[18:19]
	v_max3_f32 v41, |v18|, |v19|, |v20|
	v_max3_f32 v42, |v21|, |v22|, |v23|
	v_max3_f32 v43, |v24|, |v25|, |v26|
	v_max3_f32 v44, |v27|, |v28|, |v29|
	v_max3_f32 v48, |v30|, |v31|, |v32|
	v_max3_f32 v41, v41, v42, |v33|
	v_max3_f32 v43, v43, v44, v48
	v_max_f32_e32 v41, v41, v43
	v_pk_add_f32 v[2:3], v[2:3], v[18:19]
	v_pk_add_f32 v[4:5], v[4:5], v[20:21]
	v_max_f32_dpp v41, v41, v41 quad_perm:[1,0,3,2] row_mask:0xf bank_mask:0xf
	v_pk_add_f32 v[6:7], v[6:7], v[22:23]
	v_pk_add_f32 v[8:9], v[8:9], v[24:25]
	v_max_f32_dpp v41, v41, v41 quad_perm:[2,3,0,1] row_mask:0xf bank_mask:0xf
	v_pk_add_f32 v[10:11], v[10:11], v[26:27]
	v_pk_add_f32 v[12:13], v[12:13], v[28:29]
	v_max_f32_dpp v41, v41, v41 row_half_mirror row_mask:0xf bank_mask:0xf
	v_pk_add_f32 v[14:15], v[14:15], v[30:31]
	v_pk_add_f32 v[16:17], v[16:17], v[32:33]
	v_max_f32_dpp v41, v41, v41 row_mirror row_mask:0xf bank_mask:0xf
	s_nop 1
	v_max_f32_dpp v41, v41, v41 row_bcast:15 row_mask:0xa bank_mask:0xf
	s_nop 1
	v_max_f32_dpp v41, v41, v41 row_bcast:31 row_mask:0xc bank_mask:0xf
	s_nop 1
	v_readlane_b32 s28, v41, 63
	s_nop 1
	v_div_scale_f32 v48, s[30:31], s28, s28, v47
	v_rcp_f32_e32 v49, v48
	s_nop 0
	v_fma_f32 v50, -v48, v49, 1.0
	v_fmac_f32_e32 v49, v50, v49
	v_mov_b32_e32 v50, s28
	v_div_scale_f32 v50, vcc, s32, v50, s32
	v_mul_f32_e32 v51, v50, v49
	v_fma_f32 v52, -v48, v51, v50
	v_fmac_f32_e32 v51, v52, v49
	v_fma_f32 v48, -v48, v51, v50
	v_div_fmas_f32 v48, v48, v49, v51
	v_div_fixup_f32 v48, v48, s28, v47
	v_cmp_gt_f32_e64 vcc, s28, 0
	v_writelane_b32 v40, s28, 18
	s_nop 0
	v_cndmask_b32_e32 v48, 0, v48, vcc
	v_fmaak_f32 v49, v18, v48, 0x4b400000
	v_fmaak_f32 v50, v19, v48, 0x4b400000
	v_fmaak_f32 v51, v20, v48, 0x4b400000
	v_fmaak_f32 v52, v21, v48, 0x4b400000
	v_perm_b32 v49, v50, v49, s33
	v_perm_b32 v51, v52, v51, s34
	v_or_b32_e32 v36, v49, v51
	v_fmaak_f32 v41, v22, v48, 0x4b400000
	v_fmaak_f32 v42, v23, v48, 0x4b400000
	v_fmaak_f32 v43, v24, v48, 0x4b400000
	v_fmaak_f32 v44, v25, v48, 0x4b400000
	v_perm_b32 v41, v42, v41, s33
	v_perm_b32 v43, v44, v43, s34
	v_or_b32_e32 v37, v41, v43
	v_fmaak_f32 v49, v26, v48, 0x4b400000
	v_fmaak_f32 v50, v27, v48, 0x4b400000
	v_fmaak_f32 v51, v28, v48, 0x4b400000
	v_fmaak_f32 v52, v29, v48, 0x4b400000
	v_perm_b32 v49, v50, v49, s33
	v_perm_b32 v51, v52, v51, s34
	v_or_b32_e32 v45, v49, v51
	v_fmaak_f32 v41, v30, v48, 0x4b400000
	v_fmaak_f32 v42, v31, v48, 0x4b400000
	v_fmaak_f32 v43, v32, v48, 0x4b400000
	v_fmaak_f32 v44, v33, v48, 0x4b400000
	v_perm_b32 v41, v42, v41, s33
	v_perm_b32 v43, v44, v43, s34
	v_or_b32_e32 v46, v41, v43
	s_waitcnt vmcnt(0)
	ds_read_b128 v[18:21], v38 offset:0
	ds_read_b128 v[22:25], v38 offset:1024
	ds_read_b128 v[26:29], v38 offset:2048
	ds_read_b128 v[30:33], v38 offset:3072
	s_waitcnt lgkmcnt(0)
	s_barrier
	s_mov_b32 m0, s35
	s_nop 0
	global_load_lds_dwordx4 v34, s[16:17] nt
	global_load_lds_dwordx4 v34, s[16:17] offset:1024 nt
	global_load_lds_dwordx4 v34, s[16:17] offset:2048 nt
	global_load_lds_dwordx4 v35, s[16:17] offset:3072 nt
	s_add_u32 s16, s16, 0xfa0000
	s_addc_u32 s17, s17, 0
	v_cndmask_b32_e64 v30, 0, v30, s[18:19]
	v_cndmask_b32_e64 v31, 0, v31, s[18:19]
	v_cndmask_b32_e64 v32, 0, v32, s[18:19]
	v_cndmask_b32_e64 v33, 0, v33, s[18:19]
	v_max3_f32 v41, |v18|, |v19|, |v20|
	v_max3_f32 v42, |v21|, |v22|, |v23|
	v_max3_f32 v43, |v24|, |v25|, |v26|
	v_max3_f32 v44, |v27|, |v28|, |v29|
	v_max3_f32 v48, |v30|, |v31|, |v32|
	v_max3_f32 v41, v41, v42, |v33|
	v_max3_f32 v43, v43, v44, v48
	v_max_f32_e32 v41, v41, v43
	v_pk_add_f32 v[2:3], v[2:3], v[18:19]
	v_pk_add_f32 v[4:5], v[4:5], v[20:21]
	v_max_f32_dpp v41, v41, v41 quad_perm:[1,0,3,2] row_mask:0xf bank_mask:0xf
	v_pk_add_f32 v[6:7], v[6:7], v[22:23]
	v_pk_add_f32 v[8:9], v[8:9], v[24:25]
	v_max_f32_dpp v41, v41, v41 quad_perm:[2,3,0,1] row_mask:0xf bank_mask:0xf
	v_pk_add_f32 v[10:11], v[10:11], v[26:27]
	v_pk_add_f32 v[12:13], v[12:13], v[28:29]
	v_max_f32_dpp v41, v41, v41 row_half_mirror row_mask:0xf bank_mask:0xf
	v_pk_add_f32 v[14:15], v[14:15], v[30:31]
	v_pk_add_f32 v[16:17], v[16:17], v[32:33]
	v_max_f32_dpp v41, v41, v41 row_mirror row_mask:0xf bank_mask:0xf
	s_nop 1
	v_max_f32_dpp v41, v41, v41 row_bcast:15 row_mask:0xa bank_mask:0xf
	s_nop 1
	v_max_f32_dpp v41, v41, v41 row_bcast:31 row_mask:0xc bank_mask:0xf
	s_nop 1
	v_readlane_b32 s28, v41, 63
	s_nop 1
	v_div_scale_f32 v48, s[30:31], s28, s28, v47
	v_rcp_f32_e32 v49, v48
	s_nop 0
	v_fma_f32 v50, -v48, v49, 1.0
	v_fmac_f32_e32 v49, v50, v49
	v_mov_b32_e32 v50, s28
	v_div_scale_f32 v50, vcc, s32, v50, s32
	v_mul_f32_e32 v51, v50, v49
	v_fma_f32 v52, -v48, v51, v50
	v_fmac_f32_e32 v51, v52, v49
	v_fma_f32 v48, -v48, v51, v50
	v_div_fmas_f32 v48, v48, v49, v51
	v_div_fixup_f32 v48, v48, s28, v47
	v_cmp_gt_f32_e64 vcc, s28, 0
	v_writelane_b32 v40, s28, 19
	s_nop 0
	v_cndmask_b32_e32 v48, 0, v48, vcc
	v_fmaak_f32 v49, v18, v48, 0x4b400000
	v_fmaak_f32 v50, v19, v48, 0x4b400000
	v_fmaak_f32 v51, v20, v48, 0x4b400000
	v_fmaak_f32 v52, v21, v48, 0x4b400000
	v_perm_b32 v49, v50, v49, s33
	v_perm_b32 v51, v52, v51, s34
	v_or_b32_e32 v53, v49, v51
	v_fmaak_f32 v41, v22, v48, 0x4b400000
	v_fmaak_f32 v42, v23, v48, 0x4b400000
	v_fmaak_f32 v43, v24, v48, 0x4b400000
	v_fmaak_f32 v44, v25, v48, 0x4b400000
	v_perm_b32 v41, v42, v41, s33
	v_perm_b32 v43, v44, v43, s34
	v_or_b32_e32 v54, v41, v43
	v_fmaak_f32 v49, v26, v48, 0x4b400000
	v_fmaak_f32 v50, v27, v48, 0x4b400000
	v_fmaak_f32 v51, v28, v48, 0x4b400000
	v_fmaak_f32 v52, v29, v48, 0x4b400000
	v_perm_b32 v49, v50, v49, s33
	v_perm_b32 v51, v52, v51, s34
	v_or_b32_e32 v55, v49, v51
	v_fmaak_f32 v41, v30, v48, 0x4b400000
	v_fmaak_f32 v42, v31, v48, 0x4b400000
	v_fmaak_f32 v43, v32, v48, 0x4b400000
	v_fmaak_f32 v44, v33, v48, 0x4b400000
	v_perm_b32 v41, v42, v41, s33
	v_perm_b32 v43, v44, v43, s34
	v_or_b32_e32 v1, v41, v43
	s_waitcnt vmcnt(0)
	ds_read_b128 v[18:21], v38 offset:0
	ds_read_b128 v[22:25], v38 offset:1024
	ds_read_b128 v[26:29], v38 offset:2048
	ds_read_b128 v[30:33], v38 offset:3072
	s_waitcnt lgkmcnt(0)
	s_barrier
	s_mov_b32 m0, s35
	s_nop 0
	global_load_lds_dwordx4 v34, s[16:17] nt
	global_load_lds_dwordx4 v34, s[16:17] offset:1024 nt
	global_load_lds_dwordx4 v34, s[16:17] offset:2048 nt
	global_load_lds_dwordx4 v35, s[16:17] offset:3072 nt
	s_add_u32 s16, s16, 0xfa0000
	s_addc_u32 s17, s17, 0
	v_cndmask_b32_e64 v30, 0, v30, s[18:19]
	v_cndmask_b32_e64 v31, 0, v31, s[18:19]
	v_cndmask_b32_e64 v32, 0, v32, s[18:19]
	v_cndmask_b32_e64 v33, 0, v33, s[18:19]
	v_max3_f32 v41, |v18|, |v19|, |v20|
	v_max3_f32 v42, |v21|, |v22|, |v23|
	v_max3_f32 v43, |v24|, |v25|, |v26|
	v_max3_f32 v44, |v27|, |v28|, |v29|
	v_max3_f32 v48, |v30|, |v31|, |v32|
	v_max3_f32 v41, v41, v42, |v33|
	v_max3_f32 v43, v43, v44, v48
	v_max_f32_e32 v41, v41, v43
	v_pk_add_f32 v[2:3], v[2:3], v[18:19]
	v_pk_add_f32 v[4:5], v[4:5], v[20:21]
	v_max_f32_dpp v41, v41, v41 quad_perm:[1,0,3,2] row_mask:0xf bank_mask:0xf
	v_pk_add_f32 v[6:7], v[6:7], v[22:23]
	v_pk_add_f32 v[8:9], v[8:9], v[24:25]
	v_max_f32_dpp v41, v41, v41 quad_perm:[2,3,0,1] row_mask:0xf bank_mask:0xf
	v_pk_add_f32 v[10:11], v[10:11], v[26:27]
	v_pk_add_f32 v[12:13], v[12:13], v[28:29]
	v_max_f32_dpp v41, v41, v41 row_half_mirror row_mask:0xf bank_mask:0xf
	v_pk_add_f32 v[14:15], v[14:15], v[30:31]
	v_pk_add_f32 v[16:17], v[16:17], v[32:33]
	v_max_f32_dpp v41, v41, v41 row_mirror row_mask:0xf bank_mask:0xf
	s_nop 1
	v_max_f32_dpp v41, v41, v41 row_bcast:15 row_mask:0xa bank_mask:0xf
	s_nop 1
	v_max_f32_dpp v41, v41, v41 row_bcast:31 row_mask:0xc bank_mask:0xf
	s_nop 1
	v_readlane_b32 s28, v41, 63
	s_nop 1
	v_div_scale_f32 v48, s[30:31], s28, s28, v47
	v_rcp_f32_e32 v49, v48
	s_nop 0
	v_fma_f32 v50, -v48, v49, 1.0
	v_fmac_f32_e32 v49, v50, v49
	v_mov_b32_e32 v50, s28
	v_div_scale_f32 v50, vcc, s32, v50, s32
	v_mul_f32_e32 v51, v50, v49
	v_fma_f32 v52, -v48, v51, v50
	v_fmac_f32_e32 v51, v52, v49
	v_fma_f32 v48, -v48, v51, v50
	v_div_fmas_f32 v48, v48, v49, v51
	v_div_fixup_f32 v48, v48, s28, v47
	v_cmp_gt_f32_e64 vcc, s28, 0
	v_writelane_b32 v40, s28, 20
	s_nop 0
	v_cndmask_b32_e32 v48, 0, v48, vcc
	v_fmaak_f32 v49, v18, v48, 0x4b400000
	v_fmaak_f32 v50, v19, v48, 0x4b400000
	v_fmaak_f32 v51, v20, v48, 0x4b400000
	v_fmaak_f32 v52, v21, v48, 0x4b400000
	v_perm_b32 v49, v50, v49, s33
	v_perm_b32 v51, v52, v51, s34
	v_or_b32_e32 v49, v49, v51
	ds_write_b32 v38, v49 offset:4096
	v_fmaak_f32 v41, v22, v48, 0x4b400000
	v_fmaak_f32 v42, v23, v48, 0x4b400000
	v_fmaak_f32 v43, v24, v48, 0x4b400000
	v_fmaak_f32 v44, v25, v48, 0x4b400000
	v_perm_b32 v41, v42, v41, s33
	v_perm_b32 v43, v44, v43, s34
	v_or_b32_e32 v41, v41, v43
	ds_write_b32 v38, v41 offset:4100
	v_fmaak_f32 v49, v26, v48, 0x4b400000
	v_fmaak_f32 v50, v27, v48, 0x4b400000
	v_fmaak_f32 v51, v28, v48, 0x4b400000
	v_fmaak_f32 v52, v29, v48, 0x4b400000
	v_perm_b32 v49, v50, v49, s33
	v_perm_b32 v51, v52, v51, s34
	v_or_b32_e32 v49, v49, v51
	ds_write_b32 v38, v49 offset:4104
	v_fmaak_f32 v41, v30, v48, 0x4b400000
	v_fmaak_f32 v42, v31, v48, 0x4b400000
	v_fmaak_f32 v43, v32, v48, 0x4b400000
	v_fmaak_f32 v44, v33, v48, 0x4b400000
	v_perm_b32 v41, v42, v41, s33
	v_perm_b32 v43, v44, v43, s34
	v_or_b32_e32 v41, v41, v43
	ds_write_b32 v38, v41 offset:4108
	s_waitcnt vmcnt(0)
	ds_read_b128 v[18:21], v38 offset:0
	ds_read_b128 v[22:25], v38 offset:1024
	ds_read_b128 v[26:29], v38 offset:2048
	ds_read_b128 v[30:33], v38 offset:3072
	s_waitcnt lgkmcnt(0)
	s_barrier
	s_mov_b32 m0, s35
	s_nop 0
	global_load_lds_dwordx4 v34, s[16:17] nt
	global_load_lds_dwordx4 v34, s[16:17] offset:1024 nt
	global_load_lds_dwordx4 v34, s[16:17] offset:2048 nt
	global_load_lds_dwordx4 v35, s[16:17] offset:3072 nt
	s_add_u32 s16, s16, 0xfa0000
	s_addc_u32 s17, s17, 0
	v_cndmask_b32_e64 v30, 0, v30, s[18:19]
	v_cndmask_b32_e64 v31, 0, v31, s[18:19]
	v_cndmask_b32_e64 v32, 0, v32, s[18:19]
	v_cndmask_b32_e64 v33, 0, v33, s[18:19]
	v_max3_f32 v41, |v18|, |v19|, |v20|
	v_max3_f32 v42, |v21|, |v22|, |v23|
	v_max3_f32 v43, |v24|, |v25|, |v26|
	v_max3_f32 v44, |v27|, |v28|, |v29|
	v_max3_f32 v48, |v30|, |v31|, |v32|
	v_max3_f32 v41, v41, v42, |v33|
	v_max3_f32 v43, v43, v44, v48
	v_max_f32_e32 v41, v41, v43
	v_pk_add_f32 v[2:3], v[2:3], v[18:19]
	v_pk_add_f32 v[4:5], v[4:5], v[20:21]
	v_max_f32_dpp v41, v41, v41 quad_perm:[1,0,3,2] row_mask:0xf bank_mask:0xf
	v_pk_add_f32 v[6:7], v[6:7], v[22:23]
	v_pk_add_f32 v[8:9], v[8:9], v[24:25]
	v_max_f32_dpp v41, v41, v41 quad_perm:[2,3,0,1] row_mask:0xf bank_mask:0xf
	v_pk_add_f32 v[10:11], v[10:11], v[26:27]
	v_pk_add_f32 v[12:13], v[12:13], v[28:29]
	v_max_f32_dpp v41, v41, v41 row_half_mirror row_mask:0xf bank_mask:0xf
	v_pk_add_f32 v[14:15], v[14:15], v[30:31]
	v_pk_add_f32 v[16:17], v[16:17], v[32:33]
	v_max_f32_dpp v41, v41, v41 row_mirror row_mask:0xf bank_mask:0xf
	s_nop 1
	v_max_f32_dpp v41, v41, v41 row_bcast:15 row_mask:0xa bank_mask:0xf
	s_nop 1
	v_max_f32_dpp v41, v41, v41 row_bcast:31 row_mask:0xc bank_mask:0xf
	s_nop 1
	v_readlane_b32 s28, v41, 63
	s_nop 1
	v_div_scale_f32 v48, s[30:31], s28, s28, v47
	v_rcp_f32_e32 v49, v48
	s_nop 0
	v_fma_f32 v50, -v48, v49, 1.0
	v_fmac_f32_e32 v49, v50, v49
	v_mov_b32_e32 v50, s28
	v_div_scale_f32 v50, vcc, s32, v50, s32
	v_mul_f32_e32 v51, v50, v49
	v_fma_f32 v52, -v48, v51, v50
	v_fmac_f32_e32 v51, v52, v49
	v_fma_f32 v48, -v48, v51, v50
	v_div_fmas_f32 v48, v48, v49, v51
	v_div_fixup_f32 v48, v48, s28, v47
	v_cmp_gt_f32_e64 vcc, s28, 0
	v_writelane_b32 v40, s28, 21
	s_nop 0
	v_cndmask_b32_e32 v48, 0, v48, vcc
	v_fmaak_f32 v49, v18, v48, 0x4b400000
	v_fmaak_f32 v50, v19, v48, 0x4b400000
	v_fmaak_f32 v51, v20, v48, 0x4b400000
	v_fmaak_f32 v52, v21, v48, 0x4b400000
	v_perm_b32 v49, v50, v49, s33
	v_perm_b32 v51, v52, v51, s34
	v_or_b32_e32 v49, v49, v51
	ds_write_b32 v38, v49 offset:5120
	v_fmaak_f32 v41, v22, v48, 0x4b400000
	v_fmaak_f32 v42, v23, v48, 0x4b400000
	v_fmaak_f32 v43, v24, v48, 0x4b400000
	v_fmaak_f32 v44, v25, v48, 0x4b400000
	v_perm_b32 v41, v42, v41, s33
	v_perm_b32 v43, v44, v43, s34
	v_or_b32_e32 v41, v41, v43
	ds_write_b32 v38, v41 offset:5124
	v_fmaak_f32 v49, v26, v48, 0x4b400000
	v_fmaak_f32 v50, v27, v48, 0x4b400000
	v_fmaak_f32 v51, v28, v48, 0x4b400000
	v_fmaak_f32 v52, v29, v48, 0x4b400000
	v_perm_b32 v49, v50, v49, s33
	v_perm_b32 v51, v52, v51, s34
	v_or_b32_e32 v49, v49, v51
	ds_write_b32 v38, v49 offset:5128
	v_fmaak_f32 v41, v30, v48, 0x4b400000
	v_fmaak_f32 v42, v31, v48, 0x4b400000
	v_fmaak_f32 v43, v32, v48, 0x4b400000
	v_fmaak_f32 v44, v33, v48, 0x4b400000
	v_perm_b32 v41, v42, v41, s33
	v_perm_b32 v43, v44, v43, s34
	v_or_b32_e32 v41, v41, v43
	ds_write_b32 v38, v41 offset:5132
	s_waitcnt vmcnt(0)
	ds_read_b128 v[18:21], v38 offset:0
	ds_read_b128 v[22:25], v38 offset:1024
	ds_read_b128 v[26:29], v38 offset:2048
	ds_read_b128 v[30:33], v38 offset:3072
	s_waitcnt lgkmcnt(0)
	s_barrier
	s_mov_b32 m0, s35
	s_nop 0
	global_load_lds_dwordx4 v34, s[16:17] nt
	global_load_lds_dwordx4 v34, s[16:17] offset:1024 nt
	global_load_lds_dwordx4 v34, s[16:17] offset:2048 nt
	global_load_lds_dwordx4 v35, s[16:17] offset:3072 nt
	s_add_u32 s16, s16, 0xfa0000
	s_addc_u32 s17, s17, 0
	v_cndmask_b32_e64 v30, 0, v30, s[18:19]
	v_cndmask_b32_e64 v31, 0, v31, s[18:19]
	v_cndmask_b32_e64 v32, 0, v32, s[18:19]
	v_cndmask_b32_e64 v33, 0, v33, s[18:19]
	v_max3_f32 v41, |v18|, |v19|, |v20|
	v_max3_f32 v42, |v21|, |v22|, |v23|
	v_max3_f32 v43, |v24|, |v25|, |v26|
	v_max3_f32 v44, |v27|, |v28|, |v29|
	v_max3_f32 v48, |v30|, |v31|, |v32|
	v_max3_f32 v41, v41, v42, |v33|
	v_max3_f32 v43, v43, v44, v48
	v_max_f32_e32 v41, v41, v43
	v_pk_add_f32 v[2:3], v[2:3], v[18:19]
	v_pk_add_f32 v[4:5], v[4:5], v[20:21]
	v_max_f32_dpp v41, v41, v41 quad_perm:[1,0,3,2] row_mask:0xf bank_mask:0xf
	v_pk_add_f32 v[6:7], v[6:7], v[22:23]
	v_pk_add_f32 v[8:9], v[8:9], v[24:25]
	v_max_f32_dpp v41, v41, v41 quad_perm:[2,3,0,1] row_mask:0xf bank_mask:0xf
	v_pk_add_f32 v[10:11], v[10:11], v[26:27]
	v_pk_add_f32 v[12:13], v[12:13], v[28:29]
	v_max_f32_dpp v41, v41, v41 row_half_mirror row_mask:0xf bank_mask:0xf
	v_pk_add_f32 v[14:15], v[14:15], v[30:31]
	v_pk_add_f32 v[16:17], v[16:17], v[32:33]
	v_max_f32_dpp v41, v41, v41 row_mirror row_mask:0xf bank_mask:0xf
	s_nop 1
	v_max_f32_dpp v41, v41, v41 row_bcast:15 row_mask:0xa bank_mask:0xf
	s_nop 1
	v_max_f32_dpp v41, v41, v41 row_bcast:31 row_mask:0xc bank_mask:0xf
	s_nop 1
	v_readlane_b32 s28, v41, 63
	s_nop 1
	v_div_scale_f32 v48, s[30:31], s28, s28, v47
	v_rcp_f32_e32 v49, v48
	s_nop 0
	v_fma_f32 v50, -v48, v49, 1.0
	v_fmac_f32_e32 v49, v50, v49
	v_mov_b32_e32 v50, s28
	v_div_scale_f32 v50, vcc, s32, v50, s32
	v_mul_f32_e32 v51, v50, v49
	v_fma_f32 v52, -v48, v51, v50
	v_fmac_f32_e32 v51, v52, v49
	v_fma_f32 v48, -v48, v51, v50
	v_div_fmas_f32 v48, v48, v49, v51
	v_div_fixup_f32 v48, v48, s28, v47
	v_cmp_gt_f32_e64 vcc, s28, 0
	v_writelane_b32 v40, s28, 22
	s_nop 0
	v_cndmask_b32_e32 v48, 0, v48, vcc
	v_fmaak_f32 v49, v18, v48, 0x4b400000
	v_fmaak_f32 v50, v19, v48, 0x4b400000
	v_fmaak_f32 v51, v20, v48, 0x4b400000
	v_fmaak_f32 v52, v21, v48, 0x4b400000
	v_perm_b32 v49, v50, v49, s33
	v_perm_b32 v51, v52, v51, s34
	v_or_b32_e32 v49, v49, v51
	ds_write_b32 v38, v49 offset:6144
	v_fmaak_f32 v41, v22, v48, 0x4b400000
	v_fmaak_f32 v42, v23, v48, 0x4b400000
	v_fmaak_f32 v43, v24, v48, 0x4b400000
	v_fmaak_f32 v44, v25, v48, 0x4b400000
	v_perm_b32 v41, v42, v41, s33
	v_perm_b32 v43, v44, v43, s34
	v_or_b32_e32 v41, v41, v43
	ds_write_b32 v38, v41 offset:6148
	v_fmaak_f32 v49, v26, v48, 0x4b400000
	v_fmaak_f32 v50, v27, v48, 0x4b400000
	v_fmaak_f32 v51, v28, v48, 0x4b400000
	v_fmaak_f32 v52, v29, v48, 0x4b400000
	v_perm_b32 v49, v50, v49, s33
	v_perm_b32 v51, v52, v51, s34
	v_or_b32_e32 v49, v49, v51
	ds_write_b32 v38, v49 offset:6152
	v_fmaak_f32 v41, v30, v48, 0x4b400000
	v_fmaak_f32 v42, v31, v48, 0x4b400000
	v_fmaak_f32 v43, v32, v48, 0x4b400000
	v_fmaak_f32 v44, v33, v48, 0x4b400000
	v_perm_b32 v41, v42, v41, s33
	v_perm_b32 v43, v44, v43, s34
	v_or_b32_e32 v41, v41, v43
	ds_write_b32 v38, v41 offset:6156
	s_waitcnt vmcnt(0)
	ds_read_b128 v[18:21], v38 offset:0
	ds_read_b128 v[22:25], v38 offset:1024
	ds_read_b128 v[26:29], v38 offset:2048
	ds_read_b128 v[30:33], v38 offset:3072
	s_waitcnt lgkmcnt(0)
	s_cmp_eq_u32 s29, 1
	s_cbranch_scc0 .Lk1_nodma24
	s_mov_b32 m0, s35
	s_nop 0
	global_load_lds_dwordx4 v34, s[16:17] nt
	global_load_lds_dwordx4 v34, s[16:17] offset:1024 nt
	global_load_lds_dwordx4 v34, s[16:17] offset:2048 nt
	global_load_lds_dwordx4 v35, s[16:17] offset:3072 nt
	s_add_u32 s16, s16, 0xfa0000
	s_addc_u32 s17, s17, 0
